# rider split 16 tiles in the GQA units / 8 in the differential units
# baseline (speedup 1.0000x reference)
; DI f32x16 mfma8(v8i a, v8i b, f32x16 c) { return __builtin_amdgcn_mfma_scale_f32_32x32x64_f8f6f4(a, b, c, 0, 0, 0, 0, 0, 0); }
; DI void attn_unit_d8(unsigned char* lds, const AttnArgs& a) {
;     ...
;     auto tile = [&](const unsigned char* Kb, const unsigned char* Kn, v8i& Pa, v8i& Pb, v8i& v0, v8i& v1, const v8i& Qa, const v8i& Qb, const v8i& w0, const v8i& w1) __attribute__((always_inline)) {
;         qk(Kb, 1, s1a, s1b);
;         v0 = rd32(Kb + voff); v1 = rd32(Kb + voff + 32 * A8_PITCH);
;         o0[0] = mfma8(w0, Qa, o0[0]); o1[0] = mfma8(w0, Qb, o1[0]); o0[1] = mfma8(w1, Qa, o0[1]); o1[1] = mfma8(w1, Qb, o1[1]);
;         expsum(s0a, l0); expsum(s0b, l1); pack4(s0a, Pa, 0); pack4(s0b, Pb, 0);
;         qk(Kn, 0, s0a, s0b);
;         expsum(s1a, l0); expsum(s1b, l1); pack4(s1a, Pa, 4); pack4(s1b, Pb, 4);
; #pragma unroll
;         for (int i = 0; i < 8; ++i) { __builtin_amdgcn_sched_group_barrier(0x008, 1, 0); __builtin_amdgcn_sched_group_barrier(0x402, 22, 0); }
;     };
;     for (int t = a.t0; t < a.t1; t += 2) {
;         const int s1 = sb + 1 >= 5 ? sb - 4 : sb + 1, s2 = sb + 2 >= 5 ? sb - 3 : sb + 2, s3 = sb + 3 >= 5 ? sb - 2 : sb + 3, s4 = sb + 4 >= 5 ? sb - 1 : sb + 4;
;         { const int ta = t + 3, tb = t + 4; gload(ta < a.t1 ? ta : a.t1 - 1, kreg0, vreg0); gload(tb < a.t1 ? tb : a.t1 - 1, kreg1, vreg1); }
;         tile(lds + sb * D8_SLOT, lds + s1 * D8_SLOT, PaX, PbX, vX0, vX1, PaY, PbY, vY0, vY1);
;         tile(lds + s1 * D8_SLOT, lds + s2 * D8_SLOT, PaY, PbY, vY0, vY1, PaX, PbX, vX0, vX1);
.LBB0_663:
	s_cmp_gt_i32 s16, 3
	s_cselect_b32 s17, -4, 1
	s_add_i32 s18, s17, s16
	s_mul_i32 s6, s16, 0x2800
	s_cmp_gt_i32 s16, 2
	v_mfma_f32_32x32x64_f8f6f4 v[50:65], v[154:161], v[138:145], v[50:65]
	v_exp_f32_e32 v192, v90
	v_add_u32_e32 v90, s6, v218
	s_cselect_b32 s6, -3, 2
	s_add_i32 s6, s6, s16
	s_cmp_gt_i32 s16, 1
	s_cselect_b32 s19, -2, 3
	s_add_i32 s19, s19, s16
	s_cmp_gt_i32 s16, 0
	s_cselect_b32 s49, -1, 4
	s_min_u32 s54, s46, 64
	s_add_i32 s49, s49, s16
	s_cmp_lt_u32 s46, 61
	s_mul_i32 s17, s6, 0x2800
	s_mov_b32 s16, s6
	s_cselect_b64 s[52:53], -1, 0
	s_lshl_b32 s6, s54, 6
	s_add_i32 s54, s6, 0xc0
	s_add_i32 s55, s6, 0xfffff0c0
	s_and_b64 s[52:53], s[52:53], exec
	v_lshl_add_u64 v[98:99], v[182:183], 0, s[6:7]
	s_cselect_b32 s6, s54, s55
	s_cselect_b32 s53, s21, s48
	s_cselect_b32 s52, s20, s47
	s_min_u32 s56, s46, 63
	v_exp_f32_e32 v198, v82
	v_exp_f32_e32 v199, v83
	v_exp_f32_e32 v196, v84
	v_exp_f32_e32 v197, v85
	v_exp_f32_e32 v200, v86
	v_exp_f32_e32 v201, v87
	v_exp_f32_e32 v194, v88
	v_exp_f32_e32 v195, v89
	ds_read_b128 v[82:85], v90 offset:2560
	ds_read_b128 v[86:89], v90 offset:2576
	global_load_dwordx2 v[202:203], v[98:99], off offset:192
	v_add_u32_e32 v98, s6, v215
	s_cmp_lt_u32 s46, 60
	v_ashrrev_i32_e32 v99, 31, v98
	s_cselect_b64 s[54:55], -1, 0
	s_lshl_b32 s6, s56, 6
	v_lshlrev_b64 v[98:99], 8, v[98:99]
	s_add_i32 s56, s6, 0x100
	s_add_i32 s57, s6, 0xfffff100
	v_lshl_add_u64 v[98:99], s[52:53], 0, v[98:99]
	s_and_b64 s[52:53], s[54:55], exec
	s_cselect_b32 s54, s56, s57
	v_lshl_add_u64 v[220:221], v[98:99], 0, v[178:179]
	v_add_u32_e32 v98, s54, v215
	v_ashrrev_i32_e32 v99, 31, v98
	s_cselect_b32 s53, s21, s48
	s_cselect_b32 s52, s20, s47
	v_lshlrev_b64 v[98:99], 8, v[98:99]
	v_lshl_add_u64 v[100:101], v[182:183], 0, s[6:7]
	v_lshl_add_u64 v[98:99], s[52:53], 0, v[98:99]
	global_load_dwordx2 v[204:205], v[100:101], off offset:256
	v_lshl_add_u64 v[222:223], v[98:99], 0, v[178:179]
	s_waitcnt lgkmcnt(0)
	v_mfma_f32_32x32x64_f8f6f4 v[98:113], v[82:89], v[114:121], 0
	v_exp_f32_e32 v193, v91
	v_exp_f32_e32 v224, v92
	v_exp_f32_e32 v225, v93
	v_exp_f32_e32 v226, v94
	v_exp_f32_e32 v227, v95
	v_exp_f32_e32 v228, v96
	v_exp_f32_e32 v229, v97
	ds_read_b128 v[170:173], v90 offset:5120
	ds_read_b128 v[174:177], v90 offset:5136
	ds_read_b128 v[162:165], v90 offset:7680
	ds_read_b128 v[166:169], v90 offset:7696
	v_pk_add_f32 v[90:91], v[186:187], v[198:199]
	v_pk_add_f32 v[92:93], v[184:185], v[196:197]
	v_pk_add_f32 v[90:91], v[200:201], v[90:91]
	v_pk_add_f32 v[92:93], v[194:195], v[92:93]
	v_pk_add_f32 v[90:91], v[192:193], v[90:91]
	v_pk_add_f32 v[92:93], v[224:225], v[92:93]
	v_exp_f32_e32 v66, v66
	v_exp_f32_e32 v67, v67
	v_exp_f32_e32 v68, v68
	v_exp_f32_e32 v69, v69
	v_exp_f32_e32 v70, v70
	v_exp_f32_e32 v71, v71
	v_exp_f32_e32 v72, v72
	v_pk_add_f32 v[230:231], v[228:229], v[92:93]
	v_pk_add_f32 v[232:233], v[226:227], v[90:91]
	v_mfma_f32_32x32x64_f8f6f4 v[82:97], v[82:89], v[122:129], 0
	v_exp_f32_e32 v73, v73
	v_exp_f32_e32 v74, v74
	v_exp_f32_e32 v75, v75
	v_exp_f32_e32 v76, v76
	v_exp_f32_e32 v77, v77
	v_exp_f32_e32 v78, v78
	v_exp_f32_e32 v79, v79
	v_exp_f32_e32 v80, v80
	v_exp_f32_e32 v81, v81
	v_pk_add_f32 v[186:187], v[190:191], v[66:67]
	v_pk_add_f32 v[188:189], v[188:189], v[68:69]
	s_nop 0
	v_pk_add_f32 v[186:187], v[70:71], v[186:187]
	v_pk_add_f32 v[188:189], v[72:73], v[188:189]
	s_nop 0
	v_cvt_scalef32_pk_fp8_f32 v184, v198, v199, s36
	v_pk_add_f32 v[186:187], v[74:75], v[186:187]
	v_pk_add_f32 v[188:189], v[76:77], v[188:189]
	v_cvt_scalef32_pk_fp8_f32 v185, v200, v201, s36
	v_cvt_scalef32_pk_fp8_f32 v184, v196, v197, s36 op_sel:[0,0,0,1]
	v_pk_add_f32 v[190:191], v[78:79], v[186:187]
	v_pk_add_f32 v[188:189], v[80:81], v[188:189]
	v_mfma_f32_32x32x64_f8f6f4 v[2:17], v[154:161], v[130:137], v[2:17]
	s_nop 0
	s_nop 0
	s_nop 0
	s_nop 0
	s_nop 0
	s_nop 0
	s_mulk_i32 s18, 0x2800
	v_cvt_scalef32_pk_fp8_f32 v186, v192, v193, s36
	v_cvt_scalef32_pk_fp8_f32 v187, v226, v227, s36
	v_cvt_scalef32_pk_fp8_f32 v154, v66, v67, s36
	v_cvt_scalef32_pk_fp8_f32 v155, v70, v71, s36
	v_cvt_scalef32_pk_fp8_f32 v156, v74, v75, s36
	v_cvt_scalef32_pk_fp8_f32 v157, v78, v79, s36
	v_cvt_scalef32_pk_fp8_f32 v185, v194, v195, s36 op_sel:[0,0,0,1]
	v_add_u32_e32 v219, s18, v218
	v_cvt_scalef32_pk_fp8_f32 v186, v224, v225, s36 op_sel:[0,0,0,1]
	v_cvt_scalef32_pk_fp8_f32 v187, v228, v229, s36 op_sel:[0,0,0,1]
	v_cvt_scalef32_pk_fp8_f32 v154, v68, v69, s36 op_sel:[0,0,0,1]
	v_cvt_scalef32_pk_fp8_f32 v155, v72, v73, s36 op_sel:[0,0,0,1]
	v_cvt_scalef32_pk_fp8_f32 v156, v76, v77, s36 op_sel:[0,0,0,1]
	v_cvt_scalef32_pk_fp8_f32 v157, v80, v81, s36 op_sel:[0,0,0,1]
	v_exp_f32_e32 v98, v98
	v_exp_f32_e32 v99, v99
	v_mfma_f32_32x32x64_f8f6f4 v[34:49], v[146:153], v[138:145], v[34:49]
	v_exp_f32_e32 v100, v100
	v_exp_f32_e32 v101, v101
	v_exp_f32_e32 v102, v102
	v_exp_f32_e32 v103, v103
	v_exp_f32_e32 v104, v104
	v_exp_f32_e32 v105, v105
	v_exp_f32_e32 v106, v106
	v_exp_f32_e32 v107, v107
	v_exp_f32_e32 v108, v108
	v_exp_f32_e32 v109, v109
	v_exp_f32_e32 v110, v110
	v_exp_f32_e32 v111, v111
	v_exp_f32_e32 v112, v112
	v_exp_f32_e32 v113, v113
	ds_read_b128 v[192:195], v219
	ds_read_b128 v[196:199], v219 offset:16
	v_pk_add_f32 v[66:67], v[232:233], v[98:99]
	v_pk_add_f32 v[68:69], v[230:231], v[100:101]
	v_pk_add_f32 v[66:67], v[102:103], v[66:67]
	v_pk_add_f32 v[68:69], v[104:105], v[68:69]
	v_pk_add_f32 v[66:67], v[106:107], v[66:67]
	v_pk_add_f32 v[68:69], v[108:109], v[68:69]
	v_pk_add_f32 v[140:141], v[110:111], v[66:67]
	v_pk_add_f32 v[138:139], v[112:113], v[68:69]
	v_mfma_f32_32x32x64_f8f6f4 v[18:33], v[146:153], v[130:137], v[18:33]
	v_exp_f32_e32 v82, v82
	v_exp_f32_e32 v83, v83
	v_exp_f32_e32 v84, v84
	v_exp_f32_e32 v85, v85
	v_exp_f32_e32 v86, v86
	v_exp_f32_e32 v87, v87
	v_exp_f32_e32 v88, v88
	v_exp_f32_e32 v89, v89
	v_exp_f32_e32 v90, v90
	v_exp_f32_e32 v91, v91
	v_exp_f32_e32 v92, v92
	v_exp_f32_e32 v93, v93
	v_exp_f32_e32 v94, v94
	v_exp_f32_e32 v95, v95
	v_exp_f32_e32 v96, v96
	v_exp_f32_e32 v97, v97
	v_pk_add_f32 v[66:67], v[190:191], v[82:83]
	v_pk_add_f32 v[68:69], v[188:189], v[84:85]
	v_pk_add_f32 v[66:67], v[86:87], v[66:67]
	v_pk_add_f32 v[68:69], v[88:89], v[68:69]
	v_pk_add_f32 v[130:131], v[90:91], v[66:67]
	v_pk_add_f32 v[132:133], v[92:93], v[68:69]
	s_waitcnt lgkmcnt(0)
; DI KParamsPtr kparams() { KParamsPtr p = (KParamsPtr)__builtin_amdgcn_kernarg_segment_ptr(); asm volatile("" : "+s"(p)); return p; }
; DI f32x16 mfma8(v8i a, v8i b, f32x16 c) { return __builtin_amdgcn_mfma_scale_f32_32x32x64_f8f6f4(a, b, c, 0, 0, 0, 0, 0, 0); }
; DI void attn_unit_a8(unsigned char* lds, const AttnArgs& a) {
;     ...
;     auto w_decode = [&](int j, const float*& src, unsigned char*& dst, int& ld, int& n0, int& k0, bool& gu) __attribute__((always_inline)) {
;         const int g = (j >> 2) * 512 + a.wl, e = g / 96, rr = g - e * 96; KParamsPtr kp = kparams();
;         if (rr < 64) { src = kp->w_gu + ((size_t)a.wli * NE + e) * (1024 * 2048); dst = kp->ws + WS_WGU + (size_t)a.wli * SZ_WGU + (size_t)e * 2048 * 1024; ld = 2048; n0 = (rr & 7) * 256; k0 = ((rr >> 3) * 4 + (j & 3)) * 32; gu = true; }
;         else { const int q = rr - 64; src = kp->w_dn + ((size_t)a.wli * NE + e) * (1024 * 1024); dst = kp->ws + WS_WDN + (size_t)a.wli * SZ_WDN + (size_t)e * 1024 * 1024; ld = 1024; n0 = (q & 3) * 256; k0 = ((q >> 2) * 4 + (j & 3)) * 32; gu = false; } };
; DI void attn_unit_d8(unsigned char* lds, const AttnArgs& a) {
;     ...
;     auto tile = [&](const unsigned char* Kb, const unsigned char* Kn, v8i& Pa, v8i& Pb, v8i& v0, v8i& v1, const v8i& Qa, const v8i& Qb, const v8i& w0, const v8i& w1) __attribute__((always_inline)) {
;         qk(Kb, 1, s1a, s1b);
;         v0 = rd32(Kb + voff); v1 = rd32(Kb + voff + 32 * A8_PITCH);
;         o0[0] = mfma8(w0, Qa, o0[0]); o1[0] = mfma8(w0, Qb, o1[0]); o0[1] = mfma8(w1, Qa, o0[1]); o1[1] = mfma8(w1, Qb, o1[1]);
;         expsum(s0a, l0); expsum(s0b, l1); pack4(s0a, Pa, 0); pack4(s0b, Pb, 0);
;         qk(Kn, 0, s0a, s0b);
;         expsum(s1a, l0); expsum(s1b, l1); pack4(s1a, Pa, 4); pack4(s1b, Pb, 4);
; #pragma unroll
;         for (int i = 0; i < 8; ++i) { __builtin_amdgcn_sched_group_barrier(0x008, 1, 0); __builtin_amdgcn_sched_group_barrier(0x402, 22, 0); }
;     };
	v_mfma_f32_32x32x64_f8f6f4 v[66:81], v[192:199], v[114:121], 0
	s_nop 0
	s_nop 0
	s_nop 0
	s_nop 0
	s_nop 0
	s_nop 0
	s_nop 0
	v_cvt_scalef32_pk_fp8_f32 v188, v98, v99, s36
	v_cvt_scalef32_pk_fp8_f32 v189, v102, v103, s36
	v_cvt_scalef32_pk_fp8_f32 v190, v106, v107, s36
	v_cvt_scalef32_pk_fp8_f32 v191, v110, v111, s36
	v_cvt_scalef32_pk_fp8_f32 v158, v82, v83, s36
	v_cvt_scalef32_pk_fp8_f32 v159, v86, v87, s36
	v_pk_add_f32 v[142:143], v[96:97], v[132:133]
	v_pk_add_f32 v[144:145], v[94:95], v[130:131]
	v_cvt_scalef32_pk_fp8_f32 v160, v90, v91, s36
	v_cvt_scalef32_pk_fp8_f32 v188, v100, v101, s36 op_sel:[0,0,0,1]
	v_cvt_scalef32_pk_fp8_f32 v189, v104, v105, s36 op_sel:[0,0,0,1]
	v_cvt_scalef32_pk_fp8_f32 v190, v108, v109, s36 op_sel:[0,0,0,1]
	v_cvt_scalef32_pk_fp8_f32 v191, v112, v113, s36 op_sel:[0,0,0,1]
	v_cvt_scalef32_pk_fp8_f32 v158, v84, v85, s36 op_sel:[0,0,0,1]
	v_cvt_scalef32_pk_fp8_f32 v159, v88, v89, s36 op_sel:[0,0,0,1]
	v_mfma_f32_32x32x64_f8f6f4 v[98:113], v[192:199], v[122:129], 0
	global_load_dwordx2 v[192:193], v[220:221], off
	global_load_dwordx2 v[194:195], v[222:223], off
	ds_read_b128 v[130:133], v219 offset:2560
	ds_read_b128 v[134:137], v219 offset:2576
	s_mulk_i32 s19, 0x2800
	s_nop 0
	v_exp_f32_e32 v146, v66
	s_lshr_b32 s73, s61, 2
	v_exp_f32_e32 v147, v67
	s_add_i32 s73, s73, 4
	v_exp_f32_e32 v148, v68
	s_lshl_b32 s73, s73, 9
	v_exp_f32_e32 v149, v69
	s_add_i32 s73, s73, s42
	s_add_i32 s19, s19, 0
	v_cvt_scalef32_pk_fp8_f32 v161, v94, v95, s36
	v_exp_f32_e32 v150, v70
	s_mul_i32 s75, s73, 0xaaab
	v_exp_f32_e32 v151, v71
	s_lshr_b32 s75, s75, 22
	v_exp_f32_e32 v152, v72
	s_mul_i32 s76, s75, 0x60
	v_exp_f32_e32 v153, v73
	s_sub_i32 s76, s73, s76
	v_add_u32_e32 v224, s19, v216
	v_add_u32_e32 v225, s19, v217
	v_cvt_scalef32_pk_fp8_f32 v160, v92, v93, s36 op_sel:[0,0,0,1]
	v_cvt_scalef32_pk_fp8_f32 v161, v96, v97, s36 op_sel:[0,0,0,1]
	v_exp_f32_e32 v196, v74
	s_lshr_b32 s77, s76, 6
	v_exp_f32_e32 v197, v75
	s_lshl_b32 s78, s77, 6
	v_exp_f32_e32 v198, v76
	s_sub_i32 s76, s76, s78
	v_exp_f32_e32 v199, v77
	s_sub_i32 s78, 3, s77
	v_exp_f32_e32 v200, v78
	s_lshr_b32 s79, s76, s78
	v_exp_f32_e32 v201, v79
	s_lshl_b32 s79, s79, 2
	v_exp_f32_e32 v220, v80
	s_and_b32 s81, s61, 3
	v_exp_f32_e32 v221, v81
	s_add_i32 s79, s79, s81
	s_waitcnt lgkmcnt(0)
	v_mfma_f32_32x32x64_f8f6f4 v[82:97], v[130:137], v[114:121], 0
	v_add_f32_e64 v66, v140, v146
	v_add_f32_e64 v67, v141, v147
	v_add_f32_e64 v68, v138, v148
	v_add_f32_e64 v69, v139, v149
	v_add_f32_e64 v66, v150, v66
	v_add_f32_e64 v67, v151, v67
	v_add_f32_e64 v68, v152, v68
	v_add_f32_e64 v69, v153, v69
	v_add_f32_e64 v138, v196, v66
	v_add_f32_e64 v139, v197, v67
	v_add_f32_e64 v140, v198, v68
	v_add_f32_e64 v141, v199, v69
	v_exp_f32_e32 v98, v98
	s_lshl_b32 s79, s79, 5
	v_exp_f32_e32 v99, v99
	s_lshl_b32 s81, s63, 2
	v_exp_f32_e32 v100, v100
	s_add_i32 s81, s81, s79
	v_exp_f32_e32 v101, v101
	s_sub_i32 s78, 13, s77
	v_exp_f32_e32 v102, v102
	s_lshl_b32 s81, s81, s78
	v_exp_f32_e32 v103, v103
	s_lshr_b32 s78, 7, s77
	v_exp_f32_e32 v104, v104
	s_and_b32 s78, s76, s78
	v_exp_f32_e32 v105, v105
	s_lshl_b32 s72, s78, 10
	v_exp_f32_e32 v106, v106
	s_add_i32 s81, s81, s72
	v_exp_f32_e32 v107, v107
	s_add_i32 s72, s75, 0
	v_exp_f32_e32 v108, v108
	s_sub_i32 s80, 23, s77
	v_exp_f32_e32 v109, v109
	s_lshl_b32 s72, s72, s80
	v_exp_f32_e32 v110, v110
	s_add_i32 s81, s81, s72
	v_exp_f32_e32 v111, v111
	s_cmp_eq_u32 s77, 0
	s_cselect_b64 s[84:85], s[66:67], s[68:69]
	v_exp_f32_e32 v112, v112
	s_add_u32 s84, s84, s81
	s_addc_u32 s85, s85, 0
	v_exp_f32_e32 v113, v113
	s_lshr_b32 s80, 0x2000, s77
	v_mfma_f32_32x32x64_f8f6f4 v[66:81], v[130:137], v[122:129], 0
	v_add_f32_e64 v130, v144, v98
	v_add_f32_e64 v131, v145, v99
	v_add_f32_e64 v132, v142, v100
	v_add_f32_e64 v133, v143, v101
	v_add_f32_e64 v142, v102, v130
	v_add_f32_e64 v143, v103, v131
	v_add_f32_e64 v132, v104, v132
	v_add_f32_e64 v133, v105, v133
	v_add_f32_e64 v134, v220, v140
	v_add_f32_e64 v135, v221, v141
	v_add_f32_e64 v136, v200, v138
	v_add_f32_e64 v137, v201, v139
	s_nop 0
	s_nop 0
	s_nop 0
	s_nop 0
	s_nop 0
	s_nop 0
	v_pk_add_f32 v[142:143], v[106:107], v[142:143]
	v_pk_add_f32 v[132:133], v[108:109], v[132:133]
	v_cvt_scalef32_pk_fp8_f32 v138, v146, v147, s36
	v_cvt_scalef32_pk_fp8_f32 v139, v150, v151, s36
	v_cvt_scalef32_pk_fp8_f32 v140, v196, v197, s36
	v_cvt_scalef32_pk_fp8_f32 v141, v200, v201, s36
	v_cvt_scalef32_pk_fp8_f32 v130, v98, v99, s36
	v_cvt_scalef32_pk_fp8_f32 v131, v102, v103, s36
	v_pk_add_f32 v[146:147], v[112:113], v[132:133]
	v_pk_add_f32 v[150:151], v[110:111], v[142:143]
	v_mfma_f32_32x32x64_f8f6f4 v[50:65], v[170:177], v[184:191], v[50:65]
	v_exp_f32_e32 v82, v82
	s_and_b32 s72, s78, 3
	v_exp_f32_e32 v83, v83
	s_lshl_b32 s72, s72, 19
	v_exp_f32_e32 v84, v84
	s_lshr_b32 s81, s78, 2
	v_exp_f32_e32 v85, v85
	s_lshl_b32 s81, s81, 17
	v_add_u32_e32 v102, s17, v218
	v_exp_f32_e32 v86, v86
	s_add_i32 s72, s72, s81
	v_exp_f32_e32 v87, v87
	s_lshl_b32 s81, s78, 18
	v_exp_f32_e32 v88, v88
	s_cmp_eq_u32 s77, 0
	s_cselect_b32 s72, s72, s81
; DI void attn_unit_a8(unsigned char* lds, const AttnArgs& a) {
;     ...
;     auto w_cvt = [&]() __attribute__((always_inline)) { unsigned char* t8 = lds + AT_WT + wn4 * WPITCH + 4 * wid;
; #pragma unroll
;         for (int j = 0; j < 4; ++j) *(unsigned*)(t8 + j * WPITCH) = pk4_fp8_mul64(wq[0][j], wq[1][j], wq[2][j], wq[3][j]); };
;     const int wcol = tid >> 1, whalf = tid & 1;
;     const unsigned wper_gu = (unsigned)((wcol >> 7) * 256 + (wcol & 96) + invperm32(wcol & 31)) * 1024u + 16u * whalf;
;     const unsigned wper_dn = (unsigned)fwd_lane16(wcol) * 1024u + 16u * whalf;
;     auto w_store = [&](int j) __attribute__((always_inline)) { const float* src; unsigned char* dst; int ld, n0, k0; bool gu; w_decode(j, src, dst, ld, n0, k0, gu);
;         const int nb = n0 >> 8; const unsigned uni = (unsigned)(gu ? (nb & 3) * 512 + (nb >> 2) * 128 : nb * 256) * 1024u + (unsigned)k0;
; DI void attn_unit_d8(unsigned char* lds, const AttnArgs& a) {
;     ...
;     auto tile = [&](const unsigned char* Kb, const unsigned char* Kn, v8i& Pa, v8i& Pb, v8i& v0, v8i& v1, const v8i& Qa, const v8i& Qb, const v8i& w0, const v8i& w1) __attribute__((always_inline)) {
;         qk(Kb, 1, s1a, s1b);
;         v0 = rd32(Kb + voff); v1 = rd32(Kb + voff + 32 * A8_PITCH);
;         o0[0] = mfma8(w0, Qa, o0[0]); o1[0] = mfma8(w0, Qb, o1[0]); o0[1] = mfma8(w1, Qa, o0[1]); o1[1] = mfma8(w1, Qb, o1[1]);
;         expsum(s0a, l0); expsum(s0b, l1); pack4(s0a, Pa, 0); pack4(s0b, Pb, 0);
;         qk(Kn, 0, s0a, s0b);
;         expsum(s1a, l0); expsum(s1b, l1); pack4(s1a, Pa, 4); pack4(s1b, Pb, 4);
; #pragma unroll
;         for (int i = 0; i < 8; ++i) { __builtin_amdgcn_sched_group_barrier(0x008, 1, 0); __builtin_amdgcn_sched_group_barrier(0x402, 22, 0); }
;     };
;     for (int t = a.t0; t < a.t1; t += 2) {
;         const int s1 = sb + 1 >= 5 ? sb - 4 : sb + 1, s2 = sb + 2 >= 5 ? sb - 3 : sb + 2, s3 = sb + 3 >= 5 ? sb - 2 : sb + 3, s4 = sb + 4 >= 5 ? sb - 1 : sb + 4;
;         { const int ta = t + 3, tb = t + 4; gload(ta < a.t1 ? ta : a.t1 - 1, kreg0, vreg0); gload(tb < a.t1 ? tb : a.t1 - 1, kreg1, vreg1); }
;         tile(lds + sb * D8_SLOT, lds + s1 * D8_SLOT, PaX, PbX, vX0, vX1, PaY, PbY, vY0, vY1);
;         tile(lds + s1 * D8_SLOT, lds + s2 * D8_SLOT, PaY, PbY, vY0, vY1, PaX, PbX, vX0, vX1);
;         lstore(s3, kreg0, vreg0); lstore(s4, kreg1, vreg1);
	v_exp_f32_e32 v89, v89
	s_mul_i32 s81, s77, 0x10000000
	v_cvt_scalef32_pk_fp8_f32 v130, v100, v101, s36 op_sel:[0,0,0,1]
	v_cvt_scalef32_pk_fp8_f32 v131, v104, v105, s36 op_sel:[0,0,0,1]
	v_exp_f32_e32 v90, v90
	s_add_i32 s81, s81, 0x1094000
	v_exp_f32_e32 v91, v91
	s_add_i32 s72, s72, s79
	v_exp_f32_e32 v92, v92
	s_sub_i32 s73, 21, s77
	v_exp_f32_e32 v93, v93
	s_lshl_b32 s73, s75, s73
	ds_read_b128 v[98:101], v102
	ds_read_b128 v[102:105], v102 offset:16
	s_nop 0
	v_cvt_scalef32_pk_fp8_f32 v138, v148, v149, s36 op_sel:[0,0,0,1]
	v_cvt_scalef32_pk_fp8_f32 v139, v152, v153, s36 op_sel:[0,0,0,1]
	v_cvt_scalef32_pk_fp8_f32 v140, v198, v199, s36 op_sel:[0,0,0,1]
	v_cvt_scalef32_pk_fp8_f32 v141, v220, v221, s36 op_sel:[0,0,0,1]
	s_nop 0
	v_exp_f32_e32 v94, v94
	s_add_i32 s72, s72, s73
	v_mfma_f32_32x32x64_f8f6f4 v[2:17], v[170:177], v[154:161], v[2:17]
	v_exp_f32_e32 v148, v96
	s_add_u32 s72, s72, s81
	v_cvt_scalef32_pk_fp8_f32 v132, v106, v107, s36
	v_exp_f32_e32 v149, v97
	s_or_b32 s79, s72, s77
	v_pk_add_f32 v[96:97], v[136:137], v[82:83]
	v_pk_add_f32 v[106:107], v[134:135], v[84:85]
	v_exp_f32_e32 v66, v66
	v_exp_f32_e32 v67, v67
	v_exp_f32_e32 v68, v68
	v_exp_f32_e32 v69, v69
	v_exp_f32_e32 v95, v95
	v_cvt_scalef32_pk_fp8_f32 v133, v110, v111, s36
	v_pk_add_f32 v[106:107], v[88:89], v[106:107]
	v_pk_add_f32 v[96:97], v[86:87], v[96:97]
	v_exp_f32_e32 v70, v70
	v_exp_f32_e32 v71, v71
	v_exp_f32_e32 v72, v72
	v_exp_f32_e32 v73, v73
	v_cvt_scalef32_pk_fp8_f32 v132, v108, v109, s36 op_sel:[0,0,0,1]
	v_cvt_scalef32_pk_fp8_f32 v133, v112, v113, s36 op_sel:[0,0,0,1]
	v_pk_add_f32 v[96:97], v[90:91], v[96:97]
	v_pk_add_f32 v[106:107], v[92:93], v[106:107]
	v_exp_f32_e32 v74, v74
	v_mfma_f32_32x32x64_f8f6f4 v[34:49], v[162:169], v[184:191], v[34:49]
	v_exp_f32_e32 v75, v75
	v_exp_f32_e32 v76, v76
	v_exp_f32_e32 v77, v77
	v_exp_f32_e32 v78, v78
	v_exp_f32_e32 v79, v79
	s_nop 0
	v_exp_f32_e32 v80, v80
	v_exp_f32_e32 v81, v81
	s_nop 0
	s_nop 0
	v_cvt_scalef32_pk_fp8_f32 v142, v82, v83, s36
	s_nop 0
	v_cvt_scalef32_pk_fp8_f32 v143, v86, v87, s36
	v_cvt_scalef32_pk_fp8_f32 v144, v90, v91, s36
	v_cvt_scalef32_pk_fp8_f32 v142, v84, v85, s36 op_sel:[0,0,0,1]
	v_pk_add_f32 v[82:83], v[150:151], v[66:67]
	v_pk_add_f32 v[84:85], v[146:147], v[68:69]
	s_mulk_i32 s49, 0x2800
	v_pk_add_f32 v[184:185], v[148:149], v[106:107]
	v_pk_add_f32 v[186:187], v[94:95], v[96:97]
	v_cvt_scalef32_pk_fp8_f32 v145, v94, v95, s36
	v_cvt_scalef32_pk_fp8_f32 v143, v88, v89, s36 op_sel:[0,0,0,1]
	v_cvt_scalef32_pk_fp8_f32 v144, v92, v93, s36 op_sel:[0,0,0,1]
	v_mfma_f32_32x32x64_f8f6f4 v[18:33], v[162:169], v[154:161], v[18:33]
	v_add_f32_e64 v84, v72, v84
	v_add_f32_e64 v85, v73, v85
	v_add_f32_e64 v82, v70, v82
	v_add_f32_e64 v83, v71, v83
	s_nop 0
	s_nop 0
	s_nop 0
	s_nop 0
	s_add_i32 s6, s49, 0
	v_add_f32_e64 v82, v74, v82
	v_add_f32_e64 v83, v75, v83
	v_add_f32_e64 v84, v76, v84
	v_add_f32_e64 v85, v77, v85
	v_cvt_scalef32_pk_fp8_f32 v134, v66, v67, s36
	v_cvt_scalef32_pk_fp8_f32 v135, v70, v71, s36
	v_cvt_scalef32_pk_fp8_f32 v136, v74, v75, s36
	v_cvt_scalef32_pk_fp8_f32 v137, v78, v79, s36
	v_pk_add_f32 v[188:189], v[80:81], v[84:85]
	v_pk_add_f32 v[190:191], v[78:79], v[82:83]
	v_add_u32_e32 v106, s6, v216
	v_add_u32_e32 v107, s6, v217
	v_cvt_scalef32_pk_fp8_f32 v145, v148, v149, s36 op_sel:[0,0,0,1]
	v_cvt_scalef32_pk_fp8_f32 v134, v68, v69, s36 op_sel:[0,0,0,1]
	v_cvt_scalef32_pk_fp8_f32 v135, v72, v73, s36 op_sel:[0,0,0,1]
	v_cvt_scalef32_pk_fp8_f32 v136, v76, v77, s36 op_sel:[0,0,0,1]
	v_cvt_scalef32_pk_fp8_f32 v137, v80, v81, s36 op_sel:[0,0,0,1]
	s_waitcnt lgkmcnt(0)
	v_mfma_f32_32x32x64_f8f6f4 v[82:97], v[98:105], v[114:121], 0
	ds_read_b128 v[154:157], v219 offset:5120
	ds_read_b128 v[158:161], v219 offset:5136
	ds_read_b128 v[146:149], v219 offset:7680
	ds_read_b128 v[150:153], v219 offset:7696
	s_cmpk_gt_i32 s42, 0x1ff
	s_cbranch_scc1 .Lmy_rd0_ldum
	s_add_i32 s72, s61, -1
	s_cmp_lt_u32 s72, 8
	s_cbranch_scc0 .Lmy_rd0_noc
	s_waitcnt vmcnt(4)
	v_cvt_scalef32_pk_fp8_f32 v236, v236, v240, s62
	v_cvt_scalef32_pk_fp8_f32 v237, v237, v241, s62
	v_cvt_scalef32_pk_fp8_f32 v238, v238, v242, s62
	v_cvt_scalef32_pk_fp8_f32 v239, v239, v243, s62
	v_cvt_scalef32_pk_fp8_f32 v236, v244, v248, s62 op_sel:[0,0,0,1]
	v_cvt_scalef32_pk_fp8_f32 v237, v245, v249, s62 op_sel:[0,0,0,1]
	v_cvt_scalef32_pk_fp8_f32 v238, v246, v250, s62 op_sel:[0,0,0,1]
	v_cvt_scalef32_pk_fp8_f32 v239, v247, v251, s62 op_sel:[0,0,0,1]
	ds_write_b32 v252, v236
	ds_write_b32 v252, v237 offset:36
	ds_write_b32 v252, v238 offset:72
	ds_write_b32 v252, v239 offset:108
.Lmy_rd0_noc:
	ds_read2_b32 v[244:245], v253 offset1:1
	ds_read2_b32 v[246:247], v253 offset0:2 offset1:3
	s_cmpk_gt_i32 s42, 0x1ff
	s_cbranch_scc1 .Lmy_rd0_sdum
	s_add_i32 s72, s61, -2
	s_cmp_lt_u32 s72, 8
	s_cbranch_scc0 .Lmy_rd0_sdum
	s_andn2_b32 s73, s65, 1
	s_add_u32 s82, s70, s73
	s_addc_u32 s83, s71, 0
	s_bitcmp1_b32 s65, 0
	s_cbranch_scc1 .Lmy_rd0_sdn
	s_waitcnt lgkmcnt(0)
	global_store_dwordx4 v254, v[244:247], s[82:83]
	s_branch .Lmy_rd0_sdone

; DI void attn_unit_a8(unsigned char* lds, const AttnArgs& a) {
;     ...
;     auto w_issue = [&](int j) __attribute__((always_inline)) { const float* src; unsigned char* dst; int ld, n0, k0; bool gu; w_decode(j, src, dst, ld, n0, k0, gu);
;         const float* p = src + (size_t)(k0 + 4 * wid) * ld + n0 + wn4;
;         wq[0] = __builtin_nontemporal_load((const f32x4*)p); wq[1] = __builtin_nontemporal_load((const f32x4*)(p + ld));
;         wq[2] = __builtin_nontemporal_load((const f32x4*)(p + (size_t)2 * ld)); wq[3] = __builtin_nontemporal_load((const f32x4*)(p + (size_t)3 * ld)); };
.Lmy_rd0_sdone:
	s_cmpk_gt_i32 s42, 0x1ff
	s_cbranch_scc1 .Lmy_rd0_ld0
	s_cmp_lt_u32 s61, 8
	s_cbranch_scc1 .Lmy_rd0_lgo

; DI void attn_unit_a8(unsigned char* lds, const AttnArgs& a) {
;     ...
;     auto w_cvt = [&]() __attribute__((always_inline)) { unsigned char* t8 = lds + AT_WT + wn4 * WPITCH + 4 * wid;
; #pragma unroll
;         for (int j = 0; j < 4; ++j) *(unsigned*)(t8 + j * WPITCH) = pk4_fp8_mul64(wq[0][j], wq[1][j], wq[2][j], wq[3][j]); };
;     const int wcol = tid >> 1, whalf = tid & 1;
;     const unsigned wper_gu = (unsigned)((wcol >> 7) * 256 + (wcol & 96) + invperm32(wcol & 31)) * 1024u + 16u * whalf;
;     const unsigned wper_dn = (unsigned)fwd_lane16(wcol) * 1024u + 16u * whalf;
;     auto w_store = [&](int j) __attribute__((always_inline)) { const float* src; unsigned char* dst; int ld, n0, k0; bool gu; w_decode(j, src, dst, ld, n0, k0, gu);
;         const int nb = n0 >> 8; const unsigned uni = (unsigned)(gu ? (nb & 3) * 512 + (nb >> 2) * 128 : nb * 256) * 1024u + (unsigned)k0;
;         const unsigned off = (gu ? wper_gu : wper_dn) + uni;
;         const unsigned* t = (const unsigned*)(lds + AT_WT + wcol * WPITCH + 16 * whalf);
;         *(u32x4*)(dst + off) = (u32x4){t[0], t[1], t[2], t[3]}; };
;     ...
;     auto step = [&](int t, u32x2& kl, u32x2& vl, const u32x2& ks, const u32x2& vs, f32x16& c0, f32x16& c1, f32x16& n0, f32x16& n1, const int hk, const int wj) __attribute__((always_inline)) {
;         const int slot1 = slot == 2 ? 0 : slot + 1, slot2 = slot1 == 2 ? 0 : slot1 + 1;
;         if (hk == 1) { w_cvt(); w_issue(wj + 1 < AT_NWT ? wj + 1 : AT_NWT - 1); }
;         if (hk == 2) w_store(wj);
;         { const int tn = t + 3; gload(tn < a.t1 ? tn : a.t1 - 1, kl, vl); }
;         const unsigned char* Kb = lds + slot * AT_BUFB; const unsigned char* Kn = lds + slot1 * AT_BUFB;
;         const v8i k0 = kread(Kn, 0), k1 = kread(Kn, 1), v0 = vread(Kb, 0), v1 = vread(Kb, 1);
;         n0 = mfma8(k0, qf8, cinit); n1 = mfma8(k1, qf8, cinit);
;         expsum(c0); expsum(c1);
;         const v8i P = pack8(c0, c1);
;         o0[0] = mfma8(v0, P, o0[0]); o0[1] = mfma8(v1, P, o0[1]);
;         lstore(slot2, ks, vs);
;         __syncthreads();
;         slot = slot1;
;     };
;     {
;         int t = a.t0;
;         if (wrider)
;             for (int j = 0; j < AT_NWT; ++j, t += 2) { step(t, kregB, vregB, kregA, vregA, sx0, sx1, sy0, sy1, 1, j); step(t + 1, kregA, vregA, kregB, vregB, sy0, sy1, sx0, sx1, 2, j); }
.LBB0_702:
	s_lshl_b32 s4, s14, 1
	s_waitcnt lgkmcnt(0)
	s_lshr_b32 s12, s14, 3
	s_and_b32 s4, s4, 0x600
	s_and_b32 s12, s12, 0x80
	s_or_b32 s4, s4, s12
	s_and_b64 s[10:11], s[10:11], exec
	s_cselect_b32 s4, s4, s14
	s_and_b32 s10, s24, 3
	s_add_i32 s10, s63, s10
	s_lshl_b32 s10, s10, 5
	s_lshl_b32 s4, s4, 10
	s_add_i32 s15, s4, s10
	s_min_i32 s4, s56, 63
	s_cmp_lt_u32 s56, 60
	s_cselect_b64 s[10:11], -1, 0
	s_lshl_b32 s4, s4, 6
	v_pk_add_f32 v[48:49], v[146:147], v[110:111]
	s_add_i32 s14, s4, 0x100
	s_add_i32 s63, s4, 0xfffff100
	v_pk_add_f32 v[46:47], v[150:151], v[108:109]
	v_pk_add_f32 v[48:49], v[148:149], v[48:49]
	s_and_b64 s[12:13], s[10:11], exec
	v_pk_add_f32 v[46:47], v[142:143], v[46:47]
	v_pk_add_f32 v[48:49], v[58:59], v[48:49]
	s_cselect_b32 s12, s14, s63
	s_add_i32 s25, s25, 1
	v_pk_add_f32 v[46:47], v[144:145], v[46:47]
	v_pk_add_f32 v[48:49], v[60:61], v[48:49]
	s_and_b64 s[6:7], s[6:7], exec
	v_pk_add_f32 v[46:47], v[52:53], v[46:47]
	v_pk_add_f32 v[48:49], v[50:51], v[48:49]
	s_cselect_b32 s14, 0, s25
	v_pk_add_f32 v[46:47], v[56:57], v[46:47]
	v_pk_add_f32 v[48:49], v[54:55], v[48:49]
	s_mul_i32 s6, s14, 0x4680
	v_pk_add_f32 v[38:39], v[38:39], v[46:47]
	v_pk_add_f32 v[36:37], v[36:37], v[48:49]
	v_add_u32_e32 v48, 0xd808, v163
	v_add_u32_e32 v134, s6, v157
	v_pk_add_f32 v[50:51], v[42:43], v[38:39]
	v_pk_add_f32 v[108:109], v[40:41], v[36:37]
	v_add_u32_e32 v45, 0xd800, v163
	ds_read_b128 v[36:39], v134
	ds_read_b128 v[40:43], v134 offset:16
	ds_read2_b32 v[46:47], v45 offset1:1
	ds_read2_b32 v[48:49], v48 offset1:1
	v_pk_add_f32 v[110:111], v[34:35], v[50:51]
	v_add_u32_e32 v34, v44, v158
	v_lshl_or_b32 v34, v34, 10, v160
	v_add_u32_e32 v34, s15, v34
	s_waitcnt lgkmcnt(0)
	global_store_dwordx4 v34, v[46:49], s[8:9]
	v_add_u32_e32 v34, s12, v154
	s_and_b64 s[8:9], s[10:11], exec
	v_ashrrev_i32_e32 v35, 31, v34
	s_cselect_b32 s9, s59, s61
	s_cselect_b32 s8, s58, s60
	v_lshlrev_b64 v[34:35], 7, v[34:35]
	v_mfma_f32_32x32x64_f8f6f4 v[50:65], v[36:43], v[98:105], 0
	v_lshl_add_u64 v[42:43], s[8:9], 0, v[34:35]
	v_lshl_add_u64 v[42:43], v[42:43], 0, v[130:131]
	ds_read_b128 v[34:37], v134 offset:2560
	ds_read_b128 v[38:41], v134 offset:2576
	global_load_dwordx2 v[134:135], v[42:43], off
	v_lshl_add_u64 v[42:43], v[132:133], 0, s[4:5]
	global_load_dwordx2 v[136:137], v[42:43], off offset:256
	v_exp_f32_e32 v82, v82
	v_exp_f32_e32 v83, v83
	v_exp_f32_e32 v86, v86
	v_exp_f32_e32 v87, v87
	v_exp_f32_e32 v90, v90
	v_exp_f32_e32 v91, v91
	v_exp_f32_e32 v94, v94
	v_exp_f32_e32 v95, v95
	v_exp_f32_e32 v150, v66
	v_exp_f32_e32 v151, v67
	v_exp_f32_e32 v174, v70
	v_exp_f32_e32 v175, v71
	v_exp_f32_e32 v74, v74
	v_exp_f32_e32 v75, v75
	v_exp_f32_e32 v78, v78
	v_exp_f32_e32 v79, v79
	ds_read_b128 v[142:145], v164 offset:5120
	ds_read_b128 v[146:149], v164 offset:5136
	ds_read_b128 v[166:169], v164 offset:7680
	ds_read_b128 v[170:173], v164 offset:7696
	v_exp_f32_e32 v84, v84
	v_exp_f32_e32 v85, v85
	v_exp_f32_e32 v88, v88
	v_exp_f32_e32 v89, v89
	v_exp_f32_e32 v92, v92
	v_exp_f32_e32 v93, v93
	v_exp_f32_e32 v96, v96
	v_exp_f32_e32 v97, v97
	v_exp_f32_e32 v164, v68
	v_exp_f32_e32 v165, v69
	v_exp_f32_e32 v176, v72
	v_exp_f32_e32 v177, v73
	v_exp_f32_e32 v76, v76
	v_exp_f32_e32 v77, v77
	v_exp_f32_e32 v80, v80
	v_exp_f32_e32 v81, v81
	s_nop 0
	s_nop 0
	s_nop 0
	s_nop 0
	s_nop 0
	s_nop 0
	s_nop 0
	s_nop 0
	v_cvt_scalef32_pk_fp8_f32 v66, v82, v83, s48
	v_cvt_scalef32_pk_fp8_f32 v70, v150, v151, s48
	v_cvt_scalef32_pk_fp8_f32 v67, v86, v87, s48
	v_cvt_scalef32_pk_fp8_f32 v71, v174, v175, s48
	v_cvt_scalef32_pk_fp8_f32 v68, v90, v91, s48
	v_cvt_scalef32_pk_fp8_f32 v72, v74, v75, s48
	v_cvt_scalef32_pk_fp8_f32 v69, v94, v95, s48
	v_cvt_scalef32_pk_fp8_f32 v73, v78, v79, s48
	v_cvt_scalef32_pk_fp8_f32 v66, v84, v85, s48 op_sel:[0,0,0,1]
	v_cvt_scalef32_pk_fp8_f32 v70, v164, v165, s48 op_sel:[0,0,0,1]
	v_cvt_scalef32_pk_fp8_f32 v67, v88, v89, s48 op_sel:[0,0,0,1]
	v_cvt_scalef32_pk_fp8_f32 v71, v176, v177, s48 op_sel:[0,0,0,1]
	v_cvt_scalef32_pk_fp8_f32 v68, v92, v93, s48 op_sel:[0,0,0,1]
	v_cvt_scalef32_pk_fp8_f32 v72, v76, v77, s48 op_sel:[0,0,0,1]
	v_cvt_scalef32_pk_fp8_f32 v69, v96, v97, s48 op_sel:[0,0,0,1]
	v_cvt_scalef32_pk_fp8_f32 v73, v80, v81, s48 op_sel:[0,0,0,1]
	s_waitcnt lgkmcnt(4)
	v_mfma_f32_32x32x64_f8f6f4 v[34:49], v[34:41], v[98:105], 0
	v_add_f32_e64 v110, v110, v82
	v_add_f32_e64 v111, v111, v83
	v_add_f32_e64 v82, v108, v84
	v_add_f32_e64 v83, v109, v85
	v_add_f32_e64 v84, v86, v110
	v_add_f32_e64 v85, v87, v111
	v_add_f32_e64 v82, v88, v82
	v_add_f32_e64 v83, v89, v83
	s_addk_i32 s6, 0x4680
	v_add_f32_e64 v84, v90, v84
	v_add_f32_e64 v85, v91, v85
	v_add_f32_e64 v82, v92, v82
	v_add_f32_e64 v83, v93, v83
	s_cmp_lg_u32 s14, 2
	v_pk_add_f32 v[82:83], v[96:97], v[82:83]
	v_pk_add_f32 v[84:85], v[94:95], v[84:85]
	s_cselect_b32 s4, s6, 0
	v_pk_add_f32 v[84:85], v[150:151], v[84:85]
	v_pk_add_f32 v[82:83], v[164:165], v[82:83]
	s_add_i32 s4, s4, 0
	v_pk_add_f32 v[82:83], v[176:177], v[82:83]
	s_waitcnt lgkmcnt(2)
	v_mfma_f32_32x32x64_f8f6f4 v[18:33], v[142:149], v[66:73], v[18:33]
	v_add_f32_e64 v84, v174, v84
	v_add_f32_e64 v85, v175, v85
	v_add_f32_e64 v76, v76, v82
	v_add_f32_e64 v77, v77, v83
	v_add_f32_e64 v74, v74, v84
	v_add_f32_e64 v75, v75, v85
	s_add_i32 s24, s24, 1
	s_add_i32 s56, s56, 2
	s_addk_i32 s19, 0x80
	v_add_f32_e64 v110, v80, v76
	v_add_f32_e64 v111, v81, v77
	v_add_f32_e64 v108, v78, v74
	v_add_f32_e64 v109, v79, v75
	s_cmp_lg_u32 s24, 16
	s_waitcnt lgkmcnt(0)
	v_mfma_f32_32x32x64_f8f6f4 v[2:17], v[166:173], v[66:73], v[2:17]
	v_add_u32_e32 v66, s4, v155
	s_waitcnt vmcnt(4)
	ds_write_b64 v66, v[138:139]
	v_add_u32_e32 v66, s4, v156
	v_add_u32_e32 v66, 0x1400, v66
	s_waitcnt vmcnt(3)
	ds_write2_b32 v66, v140, v141 offset1:8
	s_waitcnt lgkmcnt(0)
	s_barrier
	s_cbranch_scc0 .LBB0_712
.LBB0_703:
	s_min_u32 s15, s24, 14
	s_add_i32 s15, s15, 1
	s_lshl_b32 s4, s15, 7
	s_and_b32 s4, s4, 0x1e00
	s_nop 0
	s_nop 0
	s_add_i32 s6, s4, s62
	v_cvt_scalef32_pk_fp8_f32 v66, v116, v112, s47
	v_cvt_scalef32_pk_fp8_f32 v67, v117, v113, s47
	s_mul_hi_u32 s4, s6, 0xaaaaaaab
	v_cvt_scalef32_pk_fp8_f32 v66, v120, v124, s47 op_sel:[0,0,0,1]
	v_cvt_scalef32_pk_fp8_f32 v67, v121, v125, s47 op_sel:[0,0,0,1]
	v_add_u32_e32 v68, 0xd800, v162
	s_lshr_b32 s4, s4, 6
	ds_write2_b32 v68, v66, v67 offset1:9
	s_nop 0
	s_nop 0
	s_mul_i32 s63, s4, 0xffffffa0
	v_cvt_scalef32_pk_fp8_f32 v66, v118, v114, s47
	v_cvt_scalef32_pk_fp8_f32 v67, v119, v115, s47
	s_add_i32 s63, s63, s6
	v_cvt_scalef32_pk_fp8_f32 v66, v122, v126, s47 op_sel:[0,0,0,1]
	v_cvt_scalef32_pk_fp8_f32 v67, v123, v127, s47 op_sel:[0,0,0,1]
	s_mov_b64 s[10:11], s[0:1]
	s_cmp_gt_i32 s63, 63
	s_mov_b64 s[12:13], -1
	ds_write2_b32 v68, v66, v67 offset0:18 offset1:27
	s_cbranch_scc0 .LBB0_705
	s_load_dwordx2 s[6:7], s[10:11], 0xc0
	s_lshl_b64 s[8:9], s[4:5], 22
	s_mov_b64 s[12:13], 0
	s_waitcnt lgkmcnt(0)
	s_add_u32 s6, s6, s8
	s_addc_u32 s7, s7, s9
	s_and_b32 s8, s63, 0x7ffffffc
	s_sub_i32 s25, s8, 64

; DI f32x16 mfma8(v8i a, v8i b, f32x16 c) { return __builtin_amdgcn_mfma_scale_f32_32x32x64_f8f6f4(a, b, c, 0, 0, 0, 0, 0, 0); }
; DI void attn_unit_d8(unsigned char* lds, const AttnArgs& a) {
;     ...
;     auto tile = [&](const unsigned char* Kb, const unsigned char* Kn, v8i& Pa, v8i& Pb, v8i& v0, v8i& v1, const v8i& Qa, const v8i& Qb, const v8i& w0, const v8i& w1) __attribute__((always_inline)) {
;         qk(Kb, 1, s1a, s1b);
;         v0 = rd32(Kb + voff); v1 = rd32(Kb + voff + 32 * A8_PITCH);
;         o0[0] = mfma8(w0, Qa, o0[0]); o1[0] = mfma8(w0, Qb, o1[0]); o0[1] = mfma8(w1, Qa, o0[1]); o1[1] = mfma8(w1, Qb, o1[1]);
;         expsum(s0a, l0); expsum(s0b, l1); pack4(s0a, Pa, 0); pack4(s0b, Pb, 0);
;         qk(Kn, 0, s0a, s0b);
;         expsum(s1a, l0); expsum(s1b, l1); pack4(s1a, Pa, 4); pack4(s1b, Pb, 4);
; #pragma unroll
;         for (int i = 0; i < 8; ++i) { __builtin_amdgcn_sched_group_barrier(0x008, 1, 0); __builtin_amdgcn_sched_group_barrier(0x402, 22, 0); }
;     };
;     for (int t = a.t0; t < a.t1; t += 2) {
;         const int s1 = sb + 1 >= 5 ? sb - 4 : sb + 1, s2 = sb + 2 >= 5 ? sb - 3 : sb + 2, s3 = sb + 3 >= 5 ? sb - 2 : sb + 3, s4 = sb + 4 >= 5 ? sb - 1 : sb + 4;
;         { const int ta = t + 3, tb = t + 4; gload(ta < a.t1 ? ta : a.t1 - 1, kreg0, vreg0); gload(tb < a.t1 ? tb : a.t1 - 1, kreg1, vreg1); }
;         tile(lds + sb * D8_SLOT, lds + s1 * D8_SLOT, PaX, PbX, vX0, vX1, PaY, PbY, vY0, vY1);
;         tile(lds + s1 * D8_SLOT, lds + s2 * D8_SLOT, PaY, PbY, vY0, vY1, PaX, PbX, vX0, vX1);
.LBB0_1888:
	s_add_i32 s22, s22, 2
	s_mul_i32 s8, s23, 0x2800
	s_cmp_gt_i32 s23, 3
	v_mfma_f32_32x32x64_f8f6f4 v[50:65], v[154:161], v[138:145], v[50:65]
	v_exp_f32_e32 v194, v90
	v_add_u32_e32 v90, s8, v219
	s_cselect_b32 s8, -4, 1
	s_add_i32 s51, s8, s23
	s_cmp_gt_i32 s23, 2
	s_cselect_b32 s8, -3, 2
	s_add_i32 s8, s8, s23
	s_cmp_gt_i32 s23, 1
	s_cselect_b32 s52, -2, 3
	s_add_i32 s52, s52, s23
	s_cmp_gt_i32 s23, 0
	s_cselect_b32 s53, -1, 4
	s_min_u32 s56, s22, 64
	s_add_i32 s53, s53, s23
	s_cmp_lt_u32 s22, 61
	s_mul_i32 s50, s8, 0x2800
	s_mov_b32 s23, s8
	s_cselect_b64 s[54:55], -1, 0
	s_lshl_b32 s8, s56, 6
	s_add_i32 s56, s8, 0xc0
	s_add_i32 s57, s8, 0xfffff0c0
	s_and_b64 s[54:55], s[54:55], exec
	v_lshl_add_u64 v[98:99], v[184:185], 0, s[8:9]
	s_cselect_b32 s8, s56, s57
	s_cselect_b32 s55, s19, s21
	s_cselect_b32 s54, s18, s20
	s_min_u32 s58, s22, 63
	v_exp_f32_e32 v200, v82
	v_exp_f32_e32 v201, v83
	v_exp_f32_e32 v198, v84
	v_exp_f32_e32 v199, v85
	v_exp_f32_e32 v202, v86
	v_exp_f32_e32 v203, v87
	v_exp_f32_e32 v196, v88
	v_exp_f32_e32 v197, v89
	ds_read_b128 v[82:85], v90 offset:2560
	ds_read_b128 v[86:89], v90 offset:2576
	global_load_dwordx2 v[204:205], v[98:99], off offset:192
	v_add_u32_e32 v98, s8, v182
	s_cmp_lt_u32 s22, 60
	v_ashrrev_i32_e32 v99, 31, v98
	s_cselect_b64 s[56:57], -1, 0
	s_lshl_b32 s8, s58, 6
	v_lshlrev_b64 v[98:99], 8, v[98:99]
	s_add_i32 s58, s8, 0x100
	s_add_i32 s59, s8, 0xfffff100
	v_lshl_add_u64 v[98:99], s[54:55], 0, v[98:99]
	s_and_b64 s[54:55], s[56:57], exec
	v_lshl_add_u64 v[100:101], v[184:185], 0, s[8:9]
	s_cselect_b32 s8, s58, s59
	v_lshl_add_u64 v[220:221], v[98:99], 0, v[178:179]
	v_add_u32_e32 v98, s8, v182
	v_ashrrev_i32_e32 v99, 31, v98
	s_cselect_b32 s55, s19, s21
	s_cselect_b32 s54, s18, s20
	v_lshlrev_b64 v[98:99], 8, v[98:99]
	v_lshl_add_u64 v[98:99], s[54:55], 0, v[98:99]
	global_load_dwordx2 v[206:207], v[100:101], off offset:256
	v_lshl_add_u64 v[222:223], v[98:99], 0, v[178:179]
	s_waitcnt lgkmcnt(0)
	v_mfma_f32_32x32x64_f8f6f4 v[98:113], v[82:89], v[114:121], 0
	v_exp_f32_e32 v195, v91
	v_exp_f32_e32 v224, v92
	v_exp_f32_e32 v225, v93
	v_exp_f32_e32 v226, v94
	v_exp_f32_e32 v227, v95
	v_exp_f32_e32 v228, v96
	v_exp_f32_e32 v229, v97
	ds_read_b128 v[170:173], v90 offset:5120
	ds_read_b128 v[174:177], v90 offset:5136
	ds_read_b128 v[162:165], v90 offset:7680
	ds_read_b128 v[166:169], v90 offset:7696
	v_pk_add_f32 v[90:91], v[188:189], v[200:201]
	v_pk_add_f32 v[92:93], v[186:187], v[198:199]
	v_pk_add_f32 v[90:91], v[202:203], v[90:91]
	v_pk_add_f32 v[92:93], v[196:197], v[92:93]
	v_pk_add_f32 v[90:91], v[194:195], v[90:91]
	v_pk_add_f32 v[92:93], v[224:225], v[92:93]
	v_exp_f32_e32 v66, v66
	v_exp_f32_e32 v67, v67
	v_exp_f32_e32 v68, v68
	v_exp_f32_e32 v69, v69
	v_exp_f32_e32 v70, v70
	v_exp_f32_e32 v71, v71
	v_exp_f32_e32 v72, v72
	v_pk_add_f32 v[230:231], v[228:229], v[92:93]
	v_pk_add_f32 v[232:233], v[226:227], v[90:91]
	v_mfma_f32_32x32x64_f8f6f4 v[82:97], v[82:89], v[122:129], 0
	v_exp_f32_e32 v73, v73
	v_exp_f32_e32 v74, v74
	v_exp_f32_e32 v75, v75
	v_exp_f32_e32 v76, v76
	v_exp_f32_e32 v77, v77
	v_exp_f32_e32 v78, v78
	v_exp_f32_e32 v79, v79
	v_exp_f32_e32 v80, v80
	v_exp_f32_e32 v81, v81
	v_pk_add_f32 v[188:189], v[192:193], v[66:67]
	v_pk_add_f32 v[190:191], v[190:191], v[68:69]
	s_nop 0
	v_pk_add_f32 v[188:189], v[70:71], v[188:189]
	v_pk_add_f32 v[190:191], v[72:73], v[190:191]
	s_nop 0
	v_cvt_scalef32_pk_fp8_f32 v186, v200, v201, s36
	v_pk_add_f32 v[188:189], v[74:75], v[188:189]
	v_pk_add_f32 v[190:191], v[76:77], v[190:191]
	v_cvt_scalef32_pk_fp8_f32 v187, v202, v203, s36
	v_cvt_scalef32_pk_fp8_f32 v186, v198, v199, s36 op_sel:[0,0,0,1]
	v_pk_add_f32 v[192:193], v[78:79], v[188:189]
	v_pk_add_f32 v[190:191], v[80:81], v[190:191]
	v_mfma_f32_32x32x64_f8f6f4 v[2:17], v[154:161], v[130:137], v[2:17]
	s_nop 0
	s_nop 0
	s_nop 0
	s_nop 0
	s_nop 0
	s_nop 0
	s_mulk_i32 s51, 0x2800
	v_cvt_scalef32_pk_fp8_f32 v188, v194, v195, s36
	v_cvt_scalef32_pk_fp8_f32 v189, v226, v227, s36
	v_cvt_scalef32_pk_fp8_f32 v154, v66, v67, s36
	v_cvt_scalef32_pk_fp8_f32 v155, v70, v71, s36
	v_cvt_scalef32_pk_fp8_f32 v156, v74, v75, s36
	v_cvt_scalef32_pk_fp8_f32 v157, v78, v79, s36
	v_cvt_scalef32_pk_fp8_f32 v187, v196, v197, s36 op_sel:[0,0,0,1]
	v_add_u32_e32 v234, s51, v219
	v_cvt_scalef32_pk_fp8_f32 v188, v224, v225, s36 op_sel:[0,0,0,1]
	v_cvt_scalef32_pk_fp8_f32 v189, v228, v229, s36 op_sel:[0,0,0,1]
	v_cvt_scalef32_pk_fp8_f32 v154, v68, v69, s36 op_sel:[0,0,0,1]
	v_cvt_scalef32_pk_fp8_f32 v155, v72, v73, s36 op_sel:[0,0,0,1]
	v_cvt_scalef32_pk_fp8_f32 v156, v76, v77, s36 op_sel:[0,0,0,1]
	v_cvt_scalef32_pk_fp8_f32 v157, v80, v81, s36 op_sel:[0,0,0,1]
	v_exp_f32_e32 v98, v98
	v_exp_f32_e32 v99, v99
	v_mfma_f32_32x32x64_f8f6f4 v[34:49], v[146:153], v[138:145], v[34:49]
	v_exp_f32_e32 v100, v100
	v_exp_f32_e32 v101, v101
	v_exp_f32_e32 v102, v102
	v_exp_f32_e32 v103, v103
	v_exp_f32_e32 v104, v104
	v_exp_f32_e32 v105, v105
	v_exp_f32_e32 v106, v106
	v_exp_f32_e32 v107, v107
	v_exp_f32_e32 v108, v108
	v_exp_f32_e32 v109, v109
	v_exp_f32_e32 v110, v110
	v_exp_f32_e32 v111, v111
	v_exp_f32_e32 v112, v112
	v_exp_f32_e32 v113, v113
	ds_read_b128 v[194:197], v234
	ds_read_b128 v[198:201], v234 offset:16
	v_pk_add_f32 v[66:67], v[232:233], v[98:99]
	v_pk_add_f32 v[68:69], v[230:231], v[100:101]
	v_pk_add_f32 v[66:67], v[102:103], v[66:67]
	v_pk_add_f32 v[68:69], v[104:105], v[68:69]
	v_pk_add_f32 v[66:67], v[106:107], v[66:67]
	v_pk_add_f32 v[68:69], v[108:109], v[68:69]
	v_pk_add_f32 v[140:141], v[110:111], v[66:67]
	v_pk_add_f32 v[138:139], v[112:113], v[68:69]
	v_mfma_f32_32x32x64_f8f6f4 v[18:33], v[146:153], v[130:137], v[18:33]
	v_exp_f32_e32 v82, v82
	v_exp_f32_e32 v83, v83
	v_exp_f32_e32 v84, v84
	v_exp_f32_e32 v85, v85
	v_exp_f32_e32 v86, v86
	v_exp_f32_e32 v87, v87
	v_exp_f32_e32 v88, v88
	v_exp_f32_e32 v89, v89
	v_exp_f32_e32 v90, v90
	v_exp_f32_e32 v91, v91
	v_exp_f32_e32 v92, v92
	v_exp_f32_e32 v93, v93
	v_exp_f32_e32 v94, v94
	v_exp_f32_e32 v95, v95
	v_exp_f32_e32 v96, v96
	v_exp_f32_e32 v97, v97
	v_pk_add_f32 v[66:67], v[192:193], v[82:83]
	v_pk_add_f32 v[68:69], v[190:191], v[84:85]
	v_pk_add_f32 v[66:67], v[86:87], v[66:67]
	v_pk_add_f32 v[68:69], v[88:89], v[68:69]
	v_pk_add_f32 v[130:131], v[90:91], v[66:67]
	v_pk_add_f32 v[132:133], v[92:93], v[68:69]
	s_waitcnt lgkmcnt(0)
; DI KParamsPtr kparams() { KParamsPtr p = (KParamsPtr)__builtin_amdgcn_kernarg_segment_ptr(); asm volatile("" : "+s"(p)); return p; }
; DI f32x16 mfma8(v8i a, v8i b, f32x16 c) { return __builtin_amdgcn_mfma_scale_f32_32x32x64_f8f6f4(a, b, c, 0, 0, 0, 0, 0, 0); }
; DI void attn_unit_a8(unsigned char* lds, const AttnArgs& a) {
;     ...
;     auto w_decode = [&](int j, const float*& src, unsigned char*& dst, int& ld, int& n0, int& k0, bool& gu) __attribute__((always_inline)) {
;         const int g = (j >> 2) * 512 + a.wl, e = g / 96, rr = g - e * 96; KParamsPtr kp = kparams();
;         if (rr < 64) { src = kp->w_gu + ((size_t)a.wli * NE + e) * (1024 * 2048); dst = kp->ws + WS_WGU + (size_t)a.wli * SZ_WGU + (size_t)e * 2048 * 1024; ld = 2048; n0 = (rr & 7) * 256; k0 = ((rr >> 3) * 4 + (j & 3)) * 32; gu = true; }
;         else { const int q = rr - 64; src = kp->w_dn + ((size_t)a.wli * NE + e) * (1024 * 1024); dst = kp->ws + WS_WDN + (size_t)a.wli * SZ_WDN + (size_t)e * 1024 * 1024; ld = 1024; n0 = (q & 3) * 256; k0 = ((q >> 2) * 4 + (j & 3)) * 32; gu = false; } };
; DI void attn_unit_d8(unsigned char* lds, const AttnArgs& a) {
;     ...
;     auto tile = [&](const unsigned char* Kb, const unsigned char* Kn, v8i& Pa, v8i& Pb, v8i& v0, v8i& v1, const v8i& Qa, const v8i& Qb, const v8i& w0, const v8i& w1) __attribute__((always_inline)) {
;         qk(Kb, 1, s1a, s1b);
;         v0 = rd32(Kb + voff); v1 = rd32(Kb + voff + 32 * A8_PITCH);
;         o0[0] = mfma8(w0, Qa, o0[0]); o1[0] = mfma8(w0, Qb, o1[0]); o0[1] = mfma8(w1, Qa, o0[1]); o1[1] = mfma8(w1, Qb, o1[1]);
;         expsum(s0a, l0); expsum(s0b, l1); pack4(s0a, Pa, 0); pack4(s0b, Pb, 0);
;         qk(Kn, 0, s0a, s0b);
;         expsum(s1a, l0); expsum(s1b, l1); pack4(s1a, Pa, 4); pack4(s1b, Pb, 4);
; #pragma unroll
;         for (int i = 0; i < 8; ++i) { __builtin_amdgcn_sched_group_barrier(0x008, 1, 0); __builtin_amdgcn_sched_group_barrier(0x402, 22, 0); }
;     };
	v_mfma_f32_32x32x64_f8f6f4 v[66:81], v[194:201], v[114:121], 0
	s_nop 0
	s_nop 0
	s_nop 0
	s_nop 0
	s_nop 0
	s_nop 0
	s_nop 0
	v_cvt_scalef32_pk_fp8_f32 v190, v98, v99, s36
	v_cvt_scalef32_pk_fp8_f32 v191, v102, v103, s36
	v_cvt_scalef32_pk_fp8_f32 v192, v106, v107, s36
	v_cvt_scalef32_pk_fp8_f32 v193, v110, v111, s36
	v_cvt_scalef32_pk_fp8_f32 v158, v82, v83, s36
	v_cvt_scalef32_pk_fp8_f32 v159, v86, v87, s36
	v_pk_add_f32 v[142:143], v[96:97], v[132:133]
	v_pk_add_f32 v[144:145], v[94:95], v[130:131]
	v_cvt_scalef32_pk_fp8_f32 v160, v90, v91, s36
	v_cvt_scalef32_pk_fp8_f32 v190, v100, v101, s36 op_sel:[0,0,0,1]
	v_cvt_scalef32_pk_fp8_f32 v191, v104, v105, s36 op_sel:[0,0,0,1]
	v_cvt_scalef32_pk_fp8_f32 v192, v108, v109, s36 op_sel:[0,0,0,1]
	v_cvt_scalef32_pk_fp8_f32 v193, v112, v113, s36 op_sel:[0,0,0,1]
	v_cvt_scalef32_pk_fp8_f32 v158, v84, v85, s36 op_sel:[0,0,0,1]
	v_cvt_scalef32_pk_fp8_f32 v159, v88, v89, s36 op_sel:[0,0,0,1]
	v_mfma_f32_32x32x64_f8f6f4 v[98:113], v[194:201], v[122:129], 0
	global_load_dwordx2 v[194:195], v[220:221], off
	global_load_dwordx2 v[196:197], v[222:223], off
	ds_read_b128 v[130:133], v234 offset:2560
	ds_read_b128 v[134:137], v234 offset:2576
	v_exp_f32_e32 v146, v66
	s_lshr_b32 s73, s61, 2
	v_exp_f32_e32 v147, v67
	s_add_i32 s73, s73, 4
	s_mulk_i32 s52, 0x2800
	s_nop 0
	s_add_i32 s8, s52, 0
	v_cvt_scalef32_pk_fp8_f32 v161, v94, v95, s36
	v_add_u32_e32 v224, s8, v183
	v_cvt_scalef32_pk_fp8_f32 v160, v92, v93, s36 op_sel:[0,0,0,1]
	v_cvt_scalef32_pk_fp8_f32 v161, v96, v97, s36 op_sel:[0,0,0,1]
	v_exp_f32_e32 v148, v68
	s_lshl_b32 s73, s73, 9
	v_exp_f32_e32 v149, v69
	s_add_i32 s73, s73, s46
	v_exp_f32_e32 v150, v70
	s_mul_i32 s75, s73, 0xaaab
	v_exp_f32_e32 v151, v71
	s_lshr_b32 s75, s75, 22
	v_exp_f32_e32 v152, v72
	s_mul_i32 s76, s75, 0x60
	v_exp_f32_e32 v153, v73
	s_sub_i32 s76, s73, s76
	v_exp_f32_e32 v198, v74
	s_lshr_b32 s77, s76, 6
	v_exp_f32_e32 v199, v75
	s_lshl_b32 s78, s77, 6
	v_exp_f32_e32 v200, v76
	s_sub_i32 s76, s76, s78
	v_exp_f32_e32 v201, v77
	s_sub_i32 s78, 3, s77
	v_exp_f32_e32 v202, v78
	s_lshr_b32 s79, s76, s78
	v_exp_f32_e32 v203, v79
	s_lshl_b32 s79, s79, 2
	v_exp_f32_e32 v220, v80
	s_and_b32 s81, s61, 3
	v_exp_f32_e32 v221, v81
	s_add_i32 s79, s79, s81
	v_pk_add_f32 v[66:67], v[140:141], v[146:147]
	s_waitcnt lgkmcnt(0)
	v_mfma_f32_32x32x64_f8f6f4 v[82:97], v[130:137], v[114:121], 0
	v_add_f32_e64 v68, v138, v148
	v_add_f32_e64 v69, v139, v149
	v_add_f32_e64 v66, v150, v66
	v_add_f32_e64 v67, v151, v67
	v_add_f32_e64 v68, v152, v68
	v_add_f32_e64 v69, v153, v69
	v_add_f32_e64 v138, v198, v66
	v_add_f32_e64 v139, v199, v67
	v_add_f32_e64 v140, v200, v68
	v_add_f32_e64 v141, v201, v69
	v_exp_f32_e32 v98, v98
	s_lshl_b32 s79, s79, 5
	v_exp_f32_e32 v99, v99
	s_lshl_b32 s81, s63, 2
	v_exp_f32_e32 v100, v100
	s_add_i32 s81, s81, s79
	v_exp_f32_e32 v101, v101
	s_sub_i32 s78, 13, s77
	v_exp_f32_e32 v102, v102
	s_lshl_b32 s81, s81, s78
	v_exp_f32_e32 v103, v103
	s_lshr_b32 s78, 7, s77
	v_exp_f32_e32 v104, v104
	s_and_b32 s78, s76, s78
	v_exp_f32_e32 v105, v105
	s_lshl_b32 s72, s78, 10
	v_exp_f32_e32 v106, v106
	s_add_i32 s81, s81, s72
	v_exp_f32_e32 v107, v107
	s_add_i32 s72, s75, 32
	v_exp_f32_e32 v108, v108
	s_sub_i32 s80, 23, s77
	v_exp_f32_e32 v109, v109
	s_lshl_b32 s72, s72, s80
	v_exp_f32_e32 v110, v110
	s_add_i32 s81, s81, s72
	v_exp_f32_e32 v111, v111
	s_cmp_eq_u32 s77, 0
	s_cselect_b64 s[84:85], s[66:67], s[68:69]
	v_exp_f32_e32 v112, v112
	s_add_u32 s84, s84, s81
	s_addc_u32 s85, s85, 0
	v_exp_f32_e32 v113, v113
	s_lshr_b32 s80, 0x2000, s77
	v_exp_f32_e32 v82, v82
	s_and_b32 s72, s78, 3
	v_mfma_f32_32x32x64_f8f6f4 v[66:81], v[130:137], v[122:129], 0
	v_add_f32_e64 v130, v144, v98
	v_add_f32_e64 v131, v145, v99
	v_add_f32_e64 v132, v142, v100
	v_add_f32_e64 v133, v143, v101
	v_add_f32_e64 v142, v102, v130
	v_add_f32_e64 v143, v103, v131
	v_add_f32_e64 v132, v104, v132
	v_add_f32_e64 v133, v105, v133
	v_add_f32_e64 v134, v220, v140
	v_add_f32_e64 v135, v221, v141
	v_add_f32_e64 v136, v202, v138
	v_add_f32_e64 v137, v203, v139
	s_nop 0
	s_nop 0
	s_nop 0
	s_nop 0
	s_nop 0
	s_nop 0
	v_pk_add_f32 v[142:143], v[106:107], v[142:143]
	v_pk_add_f32 v[132:133], v[108:109], v[132:133]
	v_cvt_scalef32_pk_fp8_f32 v138, v146, v147, s36
	v_cvt_scalef32_pk_fp8_f32 v139, v150, v151, s36
	v_cvt_scalef32_pk_fp8_f32 v140, v198, v199, s36
	v_cvt_scalef32_pk_fp8_f32 v141, v202, v203, s36
	v_cvt_scalef32_pk_fp8_f32 v130, v98, v99, s36
	v_cvt_scalef32_pk_fp8_f32 v131, v102, v103, s36
	v_pk_add_f32 v[146:147], v[112:113], v[132:133]
	v_pk_add_f32 v[150:151], v[110:111], v[142:143]
	v_mfma_f32_32x32x64_f8f6f4 v[50:65], v[170:177], v[186:193], v[50:65]
	v_exp_f32_e32 v83, v83
	s_lshl_b32 s72, s72, 19
	v_exp_f32_e32 v84, v84
	s_lshr_b32 s81, s78, 2
	v_exp_f32_e32 v85, v85
	s_lshl_b32 s81, s81, 17
	v_add_u32_e32 v102, s50, v219
	v_exp_f32_e32 v86, v86
	s_add_i32 s72, s72, s81
	v_exp_f32_e32 v87, v87
	s_lshl_b32 s81, s78, 18
	v_exp_f32_e32 v88, v88
	s_cmp_eq_u32 s77, 0
	s_cselect_b32 s72, s72, s81
; DI void attn_unit_a8(unsigned char* lds, const AttnArgs& a) {
;     ...
;     auto w_cvt = [&]() __attribute__((always_inline)) { unsigned char* t8 = lds + AT_WT + wn4 * WPITCH + 4 * wid;
; #pragma unroll
;         for (int j = 0; j < 4; ++j) *(unsigned*)(t8 + j * WPITCH) = pk4_fp8_mul64(wq[0][j], wq[1][j], wq[2][j], wq[3][j]); };
;     const int wcol = tid >> 1, whalf = tid & 1;
;     const unsigned wper_gu = (unsigned)((wcol >> 7) * 256 + (wcol & 96) + invperm32(wcol & 31)) * 1024u + 16u * whalf;
;     const unsigned wper_dn = (unsigned)fwd_lane16(wcol) * 1024u + 16u * whalf;
;     auto w_store = [&](int j) __attribute__((always_inline)) { const float* src; unsigned char* dst; int ld, n0, k0; bool gu; w_decode(j, src, dst, ld, n0, k0, gu);
;         const int nb = n0 >> 8; const unsigned uni = (unsigned)(gu ? (nb & 3) * 512 + (nb >> 2) * 128 : nb * 256) * 1024u + (unsigned)k0;
; DI void attn_unit_d8(unsigned char* lds, const AttnArgs& a) {
;     ...
;     auto tile = [&](const unsigned char* Kb, const unsigned char* Kn, v8i& Pa, v8i& Pb, v8i& v0, v8i& v1, const v8i& Qa, const v8i& Qb, const v8i& w0, const v8i& w1) __attribute__((always_inline)) {
;         qk(Kb, 1, s1a, s1b);
;         v0 = rd32(Kb + voff); v1 = rd32(Kb + voff + 32 * A8_PITCH);
;         o0[0] = mfma8(w0, Qa, o0[0]); o1[0] = mfma8(w0, Qb, o1[0]); o0[1] = mfma8(w1, Qa, o0[1]); o1[1] = mfma8(w1, Qb, o1[1]);
;         expsum(s0a, l0); expsum(s0b, l1); pack4(s0a, Pa, 0); pack4(s0b, Pb, 0);
;         qk(Kn, 0, s0a, s0b);
;         expsum(s1a, l0); expsum(s1b, l1); pack4(s1a, Pa, 4); pack4(s1b, Pb, 4);
; #pragma unroll
;         for (int i = 0; i < 8; ++i) { __builtin_amdgcn_sched_group_barrier(0x008, 1, 0); __builtin_amdgcn_sched_group_barrier(0x402, 22, 0); }
;     };
;     for (int t = a.t0; t < a.t1; t += 2) {
;         const int s1 = sb + 1 >= 5 ? sb - 4 : sb + 1, s2 = sb + 2 >= 5 ? sb - 3 : sb + 2, s3 = sb + 3 >= 5 ? sb - 2 : sb + 3, s4 = sb + 4 >= 5 ? sb - 1 : sb + 4;
;         { const int ta = t + 3, tb = t + 4; gload(ta < a.t1 ? ta : a.t1 - 1, kreg0, vreg0); gload(tb < a.t1 ? tb : a.t1 - 1, kreg1, vreg1); }
;         tile(lds + sb * D8_SLOT, lds + s1 * D8_SLOT, PaX, PbX, vX0, vX1, PaY, PbY, vY0, vY1);
;         tile(lds + s1 * D8_SLOT, lds + s2 * D8_SLOT, PaY, PbY, vY0, vY1, PaX, PbX, vX0, vX1);
;         lstore(s3, kreg0, vreg0); lstore(s4, kreg1, vreg1);
	v_exp_f32_e32 v89, v89
	s_mul_i32 s81, s77, 0xc000000
	v_cvt_scalef32_pk_fp8_f32 v130, v100, v101, s36 op_sel:[0,0,0,1]
	v_cvt_scalef32_pk_fp8_f32 v131, v104, v105, s36 op_sel:[0,0,0,1]
	v_exp_f32_e32 v90, v90
	s_add_i32 s81, s81, 0x9094000
	v_exp_f32_e32 v91, v91
	s_add_i32 s72, s72, s79
	v_exp_f32_e32 v92, v92
	s_sub_i32 s73, 21, s77
	v_exp_f32_e32 v93, v93
	s_lshl_b32 s73, s75, s73
	ds_read_b128 v[98:101], v102
	ds_read_b128 v[102:105], v102 offset:16
	s_nop 0
	v_cvt_scalef32_pk_fp8_f32 v138, v148, v149, s36 op_sel:[0,0,0,1]
	v_cvt_scalef32_pk_fp8_f32 v139, v152, v153, s36 op_sel:[0,0,0,1]
	v_cvt_scalef32_pk_fp8_f32 v140, v200, v201, s36 op_sel:[0,0,0,1]
	v_cvt_scalef32_pk_fp8_f32 v141, v220, v221, s36 op_sel:[0,0,0,1]
	s_nop 0
	v_exp_f32_e32 v94, v94
	s_add_i32 s72, s72, s73
	v_exp_f32_e32 v95, v95
	s_add_u32 s72, s72, s81
	v_mfma_f32_32x32x64_f8f6f4 v[2:17], v[170:177], v[154:161], v[2:17]
	v_exp_f32_e32 v148, v96
	s_or_b32 s79, s72, s77
	v_cvt_scalef32_pk_fp8_f32 v132, v106, v107, s36
	v_exp_f32_e32 v149, v97
	v_pk_add_f32 v[96:97], v[136:137], v[82:83]
	v_pk_add_f32 v[106:107], v[134:135], v[84:85]
	v_exp_f32_e32 v66, v66
	v_exp_f32_e32 v67, v67
	v_exp_f32_e32 v68, v68
	v_exp_f32_e32 v69, v69
	v_cvt_scalef32_pk_fp8_f32 v133, v110, v111, s36
	v_pk_add_f32 v[106:107], v[88:89], v[106:107]
	v_pk_add_f32 v[96:97], v[86:87], v[96:97]
	v_exp_f32_e32 v70, v70
	v_exp_f32_e32 v71, v71
	v_exp_f32_e32 v72, v72
	v_exp_f32_e32 v73, v73
	v_cvt_scalef32_pk_fp8_f32 v132, v108, v109, s36 op_sel:[0,0,0,1]
	v_cvt_scalef32_pk_fp8_f32 v133, v112, v113, s36 op_sel:[0,0,0,1]
	v_pk_add_f32 v[96:97], v[90:91], v[96:97]
	v_pk_add_f32 v[106:107], v[92:93], v[106:107]
	v_exp_f32_e32 v74, v74
	v_exp_f32_e32 v75, v75
	v_mfma_f32_32x32x64_f8f6f4 v[34:49], v[162:169], v[186:193], v[34:49]
	v_exp_f32_e32 v76, v76
	v_exp_f32_e32 v77, v77
	v_exp_f32_e32 v78, v78
	v_exp_f32_e32 v79, v79
	s_nop 0
	v_exp_f32_e32 v80, v80
	v_exp_f32_e32 v81, v81
	s_nop 0
	s_nop 0
	v_cvt_scalef32_pk_fp8_f32 v142, v82, v83, s36
	s_nop 0
	v_cvt_scalef32_pk_fp8_f32 v143, v86, v87, s36
	v_cvt_scalef32_pk_fp8_f32 v144, v90, v91, s36
	v_cvt_scalef32_pk_fp8_f32 v142, v84, v85, s36 op_sel:[0,0,0,1]
	v_pk_add_f32 v[82:83], v[150:151], v[66:67]
	v_pk_add_f32 v[84:85], v[146:147], v[68:69]
	s_mulk_i32 s53, 0x2800
	v_pk_add_f32 v[186:187], v[148:149], v[106:107]
	v_pk_add_f32 v[188:189], v[94:95], v[96:97]
	v_cvt_scalef32_pk_fp8_f32 v145, v94, v95, s36
	v_cvt_scalef32_pk_fp8_f32 v143, v88, v89, s36 op_sel:[0,0,0,1]
	v_cvt_scalef32_pk_fp8_f32 v144, v92, v93, s36 op_sel:[0,0,0,1]
	v_pk_add_f32 v[84:85], v[72:73], v[84:85]
	v_mfma_f32_32x32x64_f8f6f4 v[18:33], v[162:169], v[154:161], v[18:33]
	v_add_f32_e64 v82, v70, v82
	v_add_f32_e64 v83, v71, v83
	s_nop 0
	s_nop 0
	s_nop 0
	s_nop 0
	s_add_i32 s51, s53, 0
	v_add_f32_e64 v82, v74, v82
	v_add_f32_e64 v83, v75, v83
	v_add_f32_e64 v84, v76, v84
	v_add_f32_e64 v85, v77, v85
	v_cvt_scalef32_pk_fp8_f32 v134, v66, v67, s36
	v_cvt_scalef32_pk_fp8_f32 v135, v70, v71, s36
	v_cvt_scalef32_pk_fp8_f32 v136, v74, v75, s36
	v_cvt_scalef32_pk_fp8_f32 v137, v78, v79, s36
	v_pk_add_f32 v[190:191], v[80:81], v[84:85]
	v_pk_add_f32 v[192:193], v[78:79], v[82:83]
	v_add_u32_e32 v106, s8, v218
	v_add_u32_e32 v107, s51, v183
	v_cvt_scalef32_pk_fp8_f32 v145, v148, v149, s36 op_sel:[0,0,0,1]
	v_cvt_scalef32_pk_fp8_f32 v134, v68, v69, s36 op_sel:[0,0,0,1]
	v_cvt_scalef32_pk_fp8_f32 v135, v72, v73, s36 op_sel:[0,0,0,1]
	v_cvt_scalef32_pk_fp8_f32 v136, v76, v77, s36 op_sel:[0,0,0,1]
	v_cvt_scalef32_pk_fp8_f32 v137, v80, v81, s36 op_sel:[0,0,0,1]
	s_waitcnt lgkmcnt(0)
	v_mfma_f32_32x32x64_f8f6f4 v[82:97], v[98:105], v[114:121], 0
	ds_read_b128 v[154:157], v234 offset:5120
	ds_read_b128 v[158:161], v234 offset:5136
	ds_read_b128 v[146:149], v234 offset:7680
	ds_read_b128 v[150:153], v234 offset:7696
	s_cmpk_gt_i32 s46, 0x1ff
	s_cbranch_scc1 .Lmy_rd1_ldum
	s_add_i32 s72, s61, -1
	s_cmp_lt_u32 s72, 8
	s_cbranch_scc0 .Lmy_rd1_noc
	s_waitcnt vmcnt(4)
	v_cvt_scalef32_pk_fp8_f32 v236, v236, v240, s62
	v_cvt_scalef32_pk_fp8_f32 v237, v237, v241, s62
	v_cvt_scalef32_pk_fp8_f32 v238, v238, v242, s62
	v_cvt_scalef32_pk_fp8_f32 v239, v239, v243, s62
	v_cvt_scalef32_pk_fp8_f32 v236, v244, v248, s62 op_sel:[0,0,0,1]
	v_cvt_scalef32_pk_fp8_f32 v237, v245, v249, s62 op_sel:[0,0,0,1]
	v_cvt_scalef32_pk_fp8_f32 v238, v246, v250, s62 op_sel:[0,0,0,1]
	v_cvt_scalef32_pk_fp8_f32 v239, v247, v251, s62 op_sel:[0,0,0,1]
	ds_write_b32 v252, v236
	ds_write_b32 v252, v237 offset:36
	ds_write_b32 v252, v238 offset:72
	ds_write_b32 v252, v239 offset:108
.Lmy_rd1_noc:
	ds_read2_b32 v[244:245], v253 offset1:1
	ds_read2_b32 v[246:247], v253 offset0:2 offset1:3
	s_cmpk_gt_i32 s46, 0x1ff
	s_cbranch_scc1 .Lmy_rd1_sdum
	s_add_i32 s72, s61, -2
	s_cmp_lt_u32 s72, 8
	s_cbranch_scc0 .Lmy_rd1_sdum
	s_andn2_b32 s73, s65, 1
	s_add_u32 s82, s70, s73
	s_addc_u32 s83, s71, 0
	s_bitcmp1_b32 s65, 0
	s_cbranch_scc1 .Lmy_rd1_sdn
	s_waitcnt lgkmcnt(0)
	global_store_dwordx4 v254, v[244:247], s[82:83]
	s_branch .Lmy_rd1_sdone

; DI void attn_unit_a8(unsigned char* lds, const AttnArgs& a) {
;     ...
;     auto w_issue = [&](int j) __attribute__((always_inline)) { const float* src; unsigned char* dst; int ld, n0, k0; bool gu; w_decode(j, src, dst, ld, n0, k0, gu);
;         const float* p = src + (size_t)(k0 + 4 * wid) * ld + n0 + wn4;
;         wq[0] = __builtin_nontemporal_load((const f32x4*)p); wq[1] = __builtin_nontemporal_load((const f32x4*)(p + ld));
;         wq[2] = __builtin_nontemporal_load((const f32x4*)(p + (size_t)2 * ld)); wq[3] = __builtin_nontemporal_load((const f32x4*)(p + (size_t)3 * ld)); };
.Lmy_rd1_sdone:
	s_cmpk_gt_i32 s46, 0x1ff
	s_cbranch_scc1 .Lmy_rd1_ld0
	s_cmp_lt_u32 s61, 8
	s_cbranch_scc1 .Lmy_rd1_lgo

; DI void attn_unit_a8(unsigned char* lds, const AttnArgs& a) {
;     ...
;     auto w_cvt = [&]() __attribute__((always_inline)) { unsigned char* t8 = lds + AT_WT + wn4 * WPITCH + 4 * wid;
; #pragma unroll
;         for (int j = 0; j < 4; ++j) *(unsigned*)(t8 + j * WPITCH) = pk4_fp8_mul64(wq[0][j], wq[1][j], wq[2][j], wq[3][j]); };
;     const int wcol = tid >> 1, whalf = tid & 1;
;     const unsigned wper_gu = (unsigned)((wcol >> 7) * 256 + (wcol & 96) + invperm32(wcol & 31)) * 1024u + 16u * whalf;
;     const unsigned wper_dn = (unsigned)fwd_lane16(wcol) * 1024u + 16u * whalf;
;     auto w_store = [&](int j) __attribute__((always_inline)) { const float* src; unsigned char* dst; int ld, n0, k0; bool gu; w_decode(j, src, dst, ld, n0, k0, gu);
;         const int nb = n0 >> 8; const unsigned uni = (unsigned)(gu ? (nb & 3) * 512 + (nb >> 2) * 128 : nb * 256) * 1024u + (unsigned)k0;
;         const unsigned off = (gu ? wper_gu : wper_dn) + uni;
;         const unsigned* t = (const unsigned*)(lds + AT_WT + wcol * WPITCH + 16 * whalf);
;         *(u32x4*)(dst + off) = (u32x4){t[0], t[1], t[2], t[3]}; };
;     ...
;     auto step = [&](int t, u32x2& kl, u32x2& vl, const u32x2& ks, const u32x2& vs, f32x16& c0, f32x16& c1, f32x16& n0, f32x16& n1, const int hk, const int wj) __attribute__((always_inline)) {
;         const int slot1 = slot == 2 ? 0 : slot + 1, slot2 = slot1 == 2 ? 0 : slot1 + 1;
;         if (hk == 1) { w_cvt(); w_issue(wj + 1 < AT_NWT ? wj + 1 : AT_NWT - 1); }
;         if (hk == 2) w_store(wj);
;         { const int tn = t + 3; gload(tn < a.t1 ? tn : a.t1 - 1, kl, vl); }
;         const unsigned char* Kb = lds + slot * AT_BUFB; const unsigned char* Kn = lds + slot1 * AT_BUFB;
;         const v8i k0 = kread(Kn, 0), k1 = kread(Kn, 1), v0 = vread(Kb, 0), v1 = vread(Kb, 1);
;         n0 = mfma8(k0, qf8, cinit); n1 = mfma8(k1, qf8, cinit);
;         expsum(c0); expsum(c1);
;         const v8i P = pack8(c0, c1);
;         o0[0] = mfma8(v0, P, o0[0]); o0[1] = mfma8(v1, P, o0[1]);
;         lstore(slot2, ks, vs);
;         __syncthreads();
;         slot = slot1;
;     };
;     {
;         int t = a.t0;
;         if (wrider)
;             for (int j = 0; j < AT_NWT; ++j, t += 2) { step(t, kregB, vregB, kregA, vregA, sx0, sx1, sy0, sy1, 1, j); step(t + 1, kregA, vregA, kregB, vregB, sy0, sy1, sx0, sx1, 2, j); }
.LBB0_1922:
	s_lshl_b32 s8, s18, 1
	s_waitcnt lgkmcnt(0)
	s_lshr_b32 s16, s18, 3
	s_and_b32 s8, s8, 0x600
	s_and_b32 s16, s16, 0x80
	s_or_b32 s8, s8, s16
	s_and_b64 s[14:15], s[14:15], exec
	v_pk_add_f32 v[54:55], v[164:165], v[108:109]
	s_cselect_b32 s8, s8, s18
	s_and_b32 s14, s50, 3
	v_pk_add_f32 v[54:55], v[154:155], v[54:55]
	s_add_i32 s14, s52, s14
	v_pk_add_f32 v[54:55], v[158:159], v[54:55]
	s_lshl_b32 s14, s14, 5
	s_lshl_b32 s8, s8, 10
	v_pk_add_f32 v[56:57], v[160:161], v[110:111]
	v_pk_add_f32 v[46:47], v[46:47], v[54:55]
	s_add_i32 s14, s8, s14
	s_add_i32 s51, s51, 1
	v_pk_add_f32 v[56:57], v[162:163], v[56:57]
	v_pk_add_f32 v[46:47], v[50:51], v[46:47]
	s_and_b64 s[12:13], s[12:13], exec
	v_pk_add_f32 v[56:57], v[152:153], v[56:57]
	v_pk_add_f32 v[40:41], v[40:41], v[46:47]
	s_cselect_b32 s18, 0, s51
	v_pk_add_f32 v[56:57], v[156:157], v[56:57]
	v_pk_add_f32 v[50:51], v[42:43], v[40:41]
	s_mul_i32 s8, s18, 0x4680
	v_pk_add_f32 v[44:45], v[44:45], v[56:57]
	v_add_u32_e32 v58, s8, v169
	v_pk_add_f32 v[110:111], v[34:35], v[50:51]
	v_add_u32_e32 v34, 0xd800, v175
	v_pk_add_f32 v[48:49], v[48:49], v[44:45]
	ds_read_b128 v[40:43], v58
	ds_read_b128 v[44:47], v58 offset:16
	v_add_u32_e32 v35, 0xd808, v175
	ds_read2_b32 v[54:55], v34 offset1:1
	ds_read2_b32 v[56:57], v35 offset1:1
	v_add_u32_e32 v50, v52, v170
	v_lshl_or_b32 v50, v50, 10, v172
	v_add_u32_e32 v50, s14, v50
	v_exp_f32_e32 v82, v82
	s_waitcnt lgkmcnt(0)
	global_store_dwordx4 v50, v[54:57], s[10:11]
	ds_read_b128 v[50:53], v58 offset:2560
	ds_read_b128 v[54:57], v58 offset:2576
	v_add_co_u32_e32 v58, vcc, s70, v148
	v_exp_f32_e32 v83, v83
	s_nop 0
	v_addc_co_u32_e32 v59, vcc, 0, v149, vcc
	global_load_dwordx2 v[136:137], v[58:59], off
	global_load_dwordx2 v[138:139], v[150:151], off offset:256
	v_exp_f32_e32 v86, v86
	v_exp_f32_e32 v87, v87
	v_exp_f32_e32 v90, v90
	v_exp_f32_e32 v91, v91
	v_exp_f32_e32 v94, v94
	v_exp_f32_e32 v95, v95
	v_exp_f32_e32 v164, v66
	v_exp_f32_e32 v165, v67
	v_exp_f32_e32 v178, v70
	v_exp_f32_e32 v179, v71
	v_exp_f32_e32 v74, v74
	v_exp_f32_e32 v75, v75
	v_exp_f32_e32 v78, v78
	v_exp_f32_e32 v79, v79
	ds_read_b128 v[148:151], v176 offset:5120
	ds_read_b128 v[152:155], v176 offset:5136
	ds_read_b128 v[156:159], v176 offset:7680
	ds_read_b128 v[160:163], v176 offset:7696
	v_exp_f32_e32 v84, v84
	v_exp_f32_e32 v85, v85
	v_exp_f32_e32 v88, v88
	v_exp_f32_e32 v89, v89
	v_exp_f32_e32 v92, v92
	v_exp_f32_e32 v93, v93
	v_exp_f32_e32 v96, v96
	v_exp_f32_e32 v97, v97
	v_exp_f32_e32 v176, v68
	v_exp_f32_e32 v177, v69
	v_exp_f32_e32 v180, v72
	v_exp_f32_e32 v181, v73
	v_exp_f32_e32 v76, v76
	v_exp_f32_e32 v77, v77
	v_exp_f32_e32 v80, v80
	v_exp_f32_e32 v81, v81
	s_nop 0
	s_nop 0
	s_nop 0
	s_nop 0
	s_nop 0
	s_nop 0
	s_nop 0
	s_nop 0
	v_cvt_scalef32_pk_fp8_f32 v66, v82, v83, s69
	v_cvt_scalef32_pk_fp8_f32 v70, v164, v165, s69
	v_cvt_scalef32_pk_fp8_f32 v67, v86, v87, s69
	v_cvt_scalef32_pk_fp8_f32 v71, v178, v179, s69
	v_cvt_scalef32_pk_fp8_f32 v68, v90, v91, s69
	v_cvt_scalef32_pk_fp8_f32 v72, v74, v75, s69
	v_cvt_scalef32_pk_fp8_f32 v69, v94, v95, s69
	v_cvt_scalef32_pk_fp8_f32 v73, v78, v79, s69
	v_pk_add_f32 v[36:37], v[36:37], v[48:49]
	v_cvt_scalef32_pk_fp8_f32 v66, v84, v85, s69 op_sel:[0,0,0,1]
	v_cvt_scalef32_pk_fp8_f32 v70, v176, v177, s69 op_sel:[0,0,0,1]
	v_cvt_scalef32_pk_fp8_f32 v67, v88, v89, s69 op_sel:[0,0,0,1]
	v_cvt_scalef32_pk_fp8_f32 v71, v180, v181, s69 op_sel:[0,0,0,1]
	v_cvt_scalef32_pk_fp8_f32 v68, v92, v93, s69 op_sel:[0,0,0,1]
	v_cvt_scalef32_pk_fp8_f32 v72, v76, v77, s69 op_sel:[0,0,0,1]
	v_cvt_scalef32_pk_fp8_f32 v69, v96, v97, s69 op_sel:[0,0,0,1]
	v_cvt_scalef32_pk_fp8_f32 v73, v80, v81, s69 op_sel:[0,0,0,1]
	v_pk_add_f32 v[108:109], v[38:39], v[36:37]
	v_mfma_f32_32x32x64_f8f6f4 v[34:49], v[40:47], v[98:105], 0
	v_add_f32_e64 v110, v110, v82
	v_add_f32_e64 v111, v111, v83
	v_add_f32_e64 v82, v108, v84
	v_add_f32_e64 v83, v109, v85
	v_add_f32_e64 v84, v86, v110
	v_add_f32_e64 v85, v87, v111
	v_add_f32_e64 v82, v88, v82
	v_add_f32_e64 v83, v89, v83
	s_addk_i32 s8, 0x4680
	v_add_f32_e64 v84, v90, v84
	v_add_f32_e64 v85, v91, v85
	v_add_f32_e64 v82, v92, v82
	v_add_f32_e64 v83, v93, v83
	s_cmp_lg_u32 s18, 2
	v_pk_add_f32 v[82:83], v[96:97], v[82:83]
	v_pk_add_f32 v[84:85], v[94:95], v[84:85]
	s_cselect_b32 s8, s8, 0
	v_pk_add_f32 v[84:85], v[164:165], v[84:85]
	v_pk_add_f32 v[82:83], v[176:177], v[82:83]
	s_add_i32 s8, s8, 0
	v_pk_add_f32 v[82:83], v[180:181], v[82:83]
	s_waitcnt lgkmcnt(4)
	v_mfma_f32_32x32x64_f8f6f4 v[50:65], v[50:57], v[98:105], 0
	v_add_f32_e64 v84, v178, v84
	v_add_f32_e64 v85, v179, v85
	v_add_f32_e64 v76, v76, v82
	v_add_f32_e64 v77, v77, v83
	v_add_f32_e64 v74, v74, v84
	v_add_f32_e64 v75, v75, v85
	s_add_i32 s50, s50, 1
	s_addk_i32 s23, 0x80
	v_add_f32_e64 v110, v80, v76
	v_add_f32_e64 v111, v81, v77
	v_add_f32_e64 v108, v78, v74
	v_add_f32_e64 v109, v79, v75
	v_lshl_add_u64 v[140:141], v[140:141], 0, s[36:37]
	s_cmp_lg_u32 s50, 16
	v_lshl_add_u64 v[142:143], v[142:143], 0, s[38:39]
	s_waitcnt lgkmcnt(2)
	v_mfma_f32_32x32x64_f8f6f4 v[18:33], v[148:155], v[66:73], v[18:33]
	s_waitcnt lgkmcnt(0)
	v_mfma_f32_32x32x64_f8f6f4 v[2:17], v[156:163], v[66:73], v[2:17]
	v_add_u32_e32 v66, s8, v131
	s_waitcnt vmcnt(4)
	ds_write_b64 v66, v[144:145]
	v_add_u32_e32 v66, s8, v168
	v_add_u32_e32 v66, 0x1400, v66
	s_waitcnt vmcnt(3)
	ds_write2_b32 v66, v146, v147 offset1:8
	s_waitcnt lgkmcnt(0)
	s_barrier
	s_cbranch_scc0 .LBB0_1931
.LBB0_1923:
	s_min_u32 s19, s50, 14
	s_add_i32 s19, s19, 1
	s_lshl_b32 s8, s19, 7
	s_and_b32 s8, s8, 0x1e00
	s_nop 0
	s_nop 0
	s_add_i32 s10, s8, s76
	v_cvt_scalef32_pk_fp8_f32 v66, v116, v112, s66
	v_cvt_scalef32_pk_fp8_f32 v67, v117, v113, s66
	s_mul_hi_u32 s8, s10, 0xaaaaaaab
	v_cvt_scalef32_pk_fp8_f32 v66, v120, v124, s66 op_sel:[0,0,0,1]
	v_cvt_scalef32_pk_fp8_f32 v67, v121, v125, s66 op_sel:[0,0,0,1]
	v_add_u32_e32 v68, 0xd800, v174
	s_lshr_b32 s8, s8, 6
	ds_write2_b32 v68, v66, v67 offset1:9
	s_nop 0
	s_nop 0
	s_mul_i32 s52, s8, 0xffffffa0
	v_cvt_scalef32_pk_fp8_f32 v66, v118, v114, s66
	v_cvt_scalef32_pk_fp8_f32 v67, v119, v115, s66
	s_add_i32 s52, s52, s10
	v_cvt_scalef32_pk_fp8_f32 v66, v122, v126, s66 op_sel:[0,0,0,1]
	v_cvt_scalef32_pk_fp8_f32 v67, v123, v127, s66 op_sel:[0,0,0,1]
	s_mov_b64 s[14:15], s[0:1]
	s_cmp_gt_i32 s52, 63
	s_mov_b64 s[16:17], -1
	ds_write2_b32 v68, v66, v67 offset0:18 offset1:27
	s_cbranch_scc0 .LBB0_1925
	s_load_dwordx2 s[10:11], s[14:15], 0xc0
	s_lshl_b64 s[12:13], s[8:9], 22
	s_mov_b64 s[16:17], 0
	s_waitcnt lgkmcnt(0)
	s_add_u32 s10, s10, s12
	s_addc_u32 s11, s11, s13
	s_add_u32 s10, s10, 0x8000000
	s_addc_u32 s11, s11, 0
	s_and_b32 s12, s52, 0x7ffffffc
	s_sub_i32 s51, s12, 64
